# router loop: gamma loads as global loads, counted vmcnt waits instead of full drains
# baseline (speedup 1.0000x reference)
; __device__ __forceinline__ void p7_ffn_prep(const Ctx& C, bool dummy = false) {
;     ...
;     for (int u = C.bid; u < T_ / 128; u += C.G) {
;         if (C.tid < 32) cnt[C.tid] = 0;
;         __syncthreads();
;         const int row = u * 128 + C.wave * 16 + i;
;         float ssq = 0.f; { const f32x4* rp = (const f32x4*)(WSP(float, WS_ROWSS) + (size_t)row * 32);
; #pragma unroll
;           for (int k = 0; k < 8; ++k) { const f32x4 v = rp[k]; ssq += (v[0] + v[1]) + (v[2] + v[3]); } }
;         const float rstd = rsqrtf(ssq * (1.0f / D_) + EPS);
;         const _Float16* __restrict__ x1 = WSP(_Float16, WS_X1H) + (size_t)row * D_ + 8 * g4; const float* fg = C.ka->in[I_FFG] + 8 * g4; unsigned char* __restrict__ h2 = WSP(unsigned char, WS_H) + (size_t)row * D_ + 8 * g4;
;         f32x4 a0 = {0.f, 0.f, 0.f, 0.f}, a1 = {0.f, 0.f, 0.f, 0.f};
;         const int rot = ((C.bid >> 3) * 2 + (C.bid & 1)) & 63;
;     ...
;         f16x8 xq[4];
; #pragma unroll
;         for (int d = 0; d < 4; ++d) xq[d] = *(const f16x8*)(x1 + 32 * P7_RC(d));
;         bf16x8 b0hN = *(const bf16x8*)(WRH + (size_t)i * D_ + 32 * rot + 8 * g4), b1hN = *(const bf16x8*)(WRH + (size_t)(i + 16) * D_ + 32 * rot + 8 * g4), b0lN = *(const bf16x8*)(WRL + (size_t)i * D_ + 32 * rot + 8 * g4), b1lN = *(const bf16x8*)(WRL + (size_t)(i + 16) * D_ + 32 * rot + 8 * g4);
;         for (int c4 = 0; c4 < 64; c4 += 4) {
; #pragma unroll
;           for (int d = 0; d < 4; ++d) { const int cl = c4 + d, c = P7_RC(cl);
;             const f32x8 xf = __builtin_convertvector(xq[d], f32x8); const f32x4 xa = {xf[0], xf[1], xf[2], xf[3]}, xb = {xf[4], xf[5], xf[6], xf[7]}, ga = *(const f32x4*)(fg + 32 * c), gb = *(const f32x4*)(fg + 32 * c + 4);
;             const bf16x8 b0h = b0hN, b1h = b1hN, b0l = b0lN, b1l = b1lN;
;             { const int cx = P7_RC(cl + 4 < 64 ? cl + 4 : 63); xq[d] = *(const f16x8*)(x1 + 32 * cx);
;               const int cn = P7_RC(cl < 63 ? cl + 1 : cl); const size_t bn = (size_t)i * D_ + 32 * cn + 8 * g4;
;               b0hN = *(const bf16x8*)(WRH + bn); b1hN = *(const bf16x8*)(WRH + bn + (size_t)16 * D_); b0lN = *(const bf16x8*)(WRL + bn); b1lN = *(const bf16x8*)(WRL + bn + (size_t)16 * D_); }
.LBB0_896:
	s_mov_b64 s[0:1], exec
	v_readlane_b32 s2, v254, 28
	v_readlane_b32 s3, v254, 29
	s_and_b64 s[2:3], s[0:1], s[2:3]
	s_mov_b64 exec, s[2:3]
	ds_write_b32 v76, v43
	s_or_b64 exec, exec, s[0:1]
	s_lshl_b32 s0, s83, 7
	v_writelane_b32 v254, s0, 32
	v_add_u32_e32 v64, s0, v75
	v_ashrrev_i32_e32 v65, 31, v64
	v_readlane_b32 s0, v254, 34
	v_lshlrev_b64 v[2:3], 7, v[64:65]
	v_readlane_b32 s1, v254, 35
	s_waitcnt lgkmcnt(0)
	s_barrier
	v_lshl_add_u64 v[18:19], s[0:1], 0, v[2:3]
	global_load_dwordx4 v[66:69], v[18:19], off
	global_load_dwordx4 v[70:73], v[18:19], off offset:16
	global_load_dwordx4 v[84:87], v[18:19], off offset:32
	global_load_dwordx4 v[88:91], v[18:19], off offset:48
	global_load_dwordx4 v[92:95], v[18:19], off offset:64
	global_load_dwordx4 v[96:99], v[18:19], off offset:80
	global_load_dwordx4 v[100:103], v[18:19], off offset:96
	global_load_dwordx4 v[104:107], v[18:19], off offset:112
	flat_load_dwordx2 v[108:109], v[58:59] offset:160
	global_load_dwordx4 v[6:9], v[48:49], off
	global_load_dwordx4 v[2:5], v[50:51], off
	global_load_dwordx4 v[10:13], v[52:53], off
	global_load_dwordx4 v[14:17], v[54:55], off
	v_lshlrev_b64 v[18:19], 12, v[64:65]
	v_readlane_b32 s0, v254, 38
	v_lshl_add_u64 v[62:63], v[44:45], 0, v[18:19]
	v_readlane_b32 s1, v254, 39
	v_lshlrev_b64 v[64:65], 11, v[64:65]
	s_mov_b32 s6, 3
	v_lshl_add_u64 v[22:23], v[62:63], 0, s[0:1]
	v_readlane_b32 s0, v254, 40
	v_readlane_b32 s1, v254, 41
	v_readlane_b32 s7, v254, 36
	v_lshl_add_u64 v[64:65], v[46:47], 0, v[64:65]
	v_lshl_add_u64 v[24:25], v[62:63], 0, s[0:1]
	v_readlane_b32 s0, v254, 54
	v_readlane_b32 s1, v254, 55
	s_waitcnt vmcnt(0)
	v_mov_b32_e32 v110, v66
	v_lshl_add_u64 v[38:39], v[62:63], 0, s[0:1]
	v_readlane_b32 s0, v254, 56
	v_readlane_b32 s1, v254, 57
	v_mov_b32_e32 v111, v70
	v_mov_b32_e32 v70, v67
	v_lshl_add_u64 v[40:41], v[62:63], 0, s[0:1]
	global_load_dwordx4 v[34:37], v[22:23], off
	global_load_dwordx4 v[30:33], v[24:25], off
	global_load_dwordx4 v[26:29], v[38:39], off
	global_load_dwordx4 v[18:21], v[40:41], off
	v_mov_b32_e32 v66, v68
	v_mov_b32_e32 v67, v72
	v_mov_b32_e32 v72, v69
	v_mov_b32_e32 v68, v85
	v_mov_b32_e32 v69, v86
	v_mov_b32_e32 v85, v87
	v_pk_add_f32 v[70:71], v[110:111], v[70:71]
	v_pk_add_f32 v[66:67], v[66:67], v[72:73]
	v_pk_add_f32 v[68:69], v[68:69], v[84:85]
	v_pk_add_f32 v[66:67], v[70:71], v[66:67]
	v_pk_add_f32 v[68:69], v[68:69], v[68:69] op_sel:[0,1] op_sel_hi:[1,0]
	v_add_f32_e32 v41, 0, v66
	v_add_f32_e32 v86, v88, v89
	v_add_f32_e32 v88, v90, v91
	v_mov_b32_e32 v91, v92
	v_mov_b32_e32 v87, v94
	v_mov_b32_e32 v89, v95
	v_mov_b32_e32 v69, v93
	v_add_f32_e32 v90, v41, v67
	v_mov_b32_e32 v94, v97
	v_mov_b32_e32 v95, v98
	v_mov_b32_e32 v97, v99
	v_pk_add_f32 v[72:73], v[86:87], v[88:89]
	v_pk_add_f32 v[66:67], v[90:91], v[68:69]
	v_pk_add_f32 v[84:85], v[94:95], v[96:97]
	v_pk_add_f32 v[66:67], v[66:67], v[72:73]
	v_pk_add_f32 v[70:71], v[84:85], v[84:85] op_sel:[0,1] op_sel_hi:[1,0]
	v_pk_add_f32 v[66:67], v[66:67], v[66:67] op_sel:[0,1] op_sel_hi:[1,0]
	v_add_f32_e32 v98, v100, v101
	v_add_f32_e32 v100, v102, v103
	v_mov_b32_e32 v99, v106
	v_mov_b32_e32 v101, v107
	v_mov_b32_e32 v71, v105
	v_mov_b32_e32 v67, v104
	v_pk_add_f32 v[86:87], v[98:99], v[100:101]
	v_pk_add_f32 v[66:67], v[66:67], v[70:71]
	s_mov_b32 s0, 0x800000
	v_pk_add_f32 v[66:67], v[66:67], v[86:87]
	v_mov_b32_e32 v22, 0
	v_add_f32_e32 v41, v66, v67
	v_fmamk_f32 v41, v41, 0x3a000000, v78
	v_mul_f32_e32 v42, 0x4b800000, v41
	v_cmp_gt_f32_e32 vcc, s0, v41
	v_mov_b32_e32 v23, v22
	v_mov_b32_e32 v24, v22
	v_cndmask_b32_e32 v41, v41, v42, vcc
	v_rsq_f32_e32 v41, v41
	v_mov_b32_e32 v25, v22
	v_mov_b32_e32 v38, v22
	v_mov_b32_e32 v39, v22
	v_mul_f32_e32 v42, 0x45800000, v41
	v_mov_b32_e32 v40, v22
	s_waitcnt vmcnt(0) lgkmcnt(0)
	v_lshl_add_u64 v[66:67], v[108:109], 0, v[60:61]
	v_cndmask_b32_e32 v83, v41, v42, vcc
	v_mov_b32_e32 v41, v22
.LBB0_899:
	s_add_i32 s0, s7, 0xffffffa0
	s_sub_i32 s3, s7, 64
	s_add_i32 s4, s6, -2
	s_add_i32 s10, s6, -1
	s_min_u32 s12, s6, 59
	s_and_b32 s90, s0, 0x7e0
	s_mov_b32 s13, s91
	s_and_b32 s14, s3, 0x7e0
	s_min_u32 s3, s4, 59
	s_min_u32 s4, s10, 59
	s_add_i32 s10, s12, s85
	s_lshl_b32 s12, s90, 2
	s_waitcnt vmcnt(5)
	v_cvt_f32_f16_sdwa v138, v27 dst_sel:DWORD dst_unused:UNUSED_PAD src0_sel:WORD_1
	v_cvt_f32_f16_sdwa v139, v26 dst_sel:DWORD dst_unused:UNUSED_PAD src0_sel:WORD_1
	v_cvt_f32_f16_e32 v142, v27
	v_cvt_f32_f16_e32 v143, v26
	s_waitcnt vmcnt(5)
; __device__ __forceinline__ void p7_ffn_prep(const Ctx& C, bool dummy = false) {
;     ...
;         for (int c4 = 0; c4 < 64; c4 += 4) {
; #pragma unroll
;           for (int d = 0; d < 4; ++d) { const int cl = c4 + d, c = P7_RC(cl);
;             const f32x8 xf = __builtin_convertvector(xq[d], f32x8); const f32x4 xa = {xf[0], xf[1], xf[2], xf[3]}, xb = {xf[4], xf[5], xf[6], xf[7]}, ga = *(const f32x4*)(fg + 32 * c), gb = *(const f32x4*)(fg + 32 * c + 4);
;             const bf16x8 b0h = b0hN, b1h = b1hN, b0l = b0lN, b1l = b1lN;
;             { const int cx = P7_RC(cl + 4 < 64 ? cl + 4 : 63); xq[d] = *(const f16x8*)(x1 + 32 * cx);
;               const int cn = P7_RC(cl < 63 ? cl + 1 : cl); const size_t bn = (size_t)i * D_ + 32 * cn + 8 * g4;
;               b0hN = *(const bf16x8*)(WRH + bn); b1hN = *(const bf16x8*)(WRH + bn + (size_t)16 * D_); b0lN = *(const bf16x8*)(WRL + bn); b1lN = *(const bf16x8*)(WRL + bn + (size_t)16 * D_); }
;             float h[8]; h[0] = xa[0] * ga[0] * rstd; h[1] = xa[1] * ga[1] * rstd; h[2] = xa[2] * ga[2] * rstd; h[3] = xa[3] * ga[3] * rstd; h[4] = xb[0] * gb[0] * rstd; h[5] = xb[1] * gb[1] * rstd; h[6] = xb[2] * gb[2] * rstd; h[7] = xb[3] * gb[3] * rstd;
;             u32x4 hi; hi.x = cvt_pk_bf16(h[0], h[1]); hi.y = cvt_pk_bf16(h[2], h[3]); hi.z = cvt_pk_bf16(h[4], h[5]); hi.w = cvt_pk_bf16(h[6], h[7]);
;             { u32x2 w8; w8.x = pk4_fp8(h[0], h[1], h[2], h[3]); w8.y = pk4_fp8(h[4], h[5], h[6], h[7]); *(u32x2*)(h2 + 32 * c) = w8; }
;             u32x4 lo; lo.x = cvt_pk_bf16(h[0] - __uint_as_float(hi.x << 16), h[1] - __uint_as_float(hi.x & 0xFFFF0000u)); lo.y = cvt_pk_bf16(h[2] - __uint_as_float(hi.y << 16), h[3] - __uint_as_float(hi.y & 0xFFFF0000u));
;             lo.z = cvt_pk_bf16(h[4] - __uint_as_float(hi.z << 16), h[5] - __uint_as_float(hi.z & 0xFFFF0000u)); lo.w = cvt_pk_bf16(h[6] - __uint_as_float(hi.w << 16), h[7] - __uint_as_float(hi.w & 0xFFFF0000u));
;             const bf16x8 ah = __builtin_bit_cast(bf16x8, hi), al = __builtin_bit_cast(bf16x8, lo);
;             a0 = __builtin_amdgcn_mfma_f32_16x16x32_bf16(ah, b0h, a0, 0, 0, 0); a0 = __builtin_amdgcn_mfma_f32_16x16x32_bf16(ah, b0l, a0, 0, 0, 0); a0 = __builtin_amdgcn_mfma_f32_16x16x32_bf16(al, b0h, a0, 0, 0, 0);
	v_cvt_f32_f16_sdwa v147, v18 dst_sel:DWORD dst_unused:UNUSED_PAD src0_sel:WORD_1
	v_cvt_f32_f16_e32 v151, v18
	v_or_b32_e32 v18, s14, v77
	v_lshl_add_u64 v[26:27], v[66:67], 0, s[12:13]
	v_cvt_f32_f16_sdwa v136, v29 dst_sel:DWORD dst_unused:UNUSED_PAD src0_sel:WORD_1
	v_cvt_f32_f16_sdwa v137, v28 dst_sel:DWORD dst_unused:UNUSED_PAD src0_sel:WORD_1
	v_cvt_f32_f16_e32 v140, v29
	v_cvt_f32_f16_e32 v141, v28
	v_cvt_f32_f16_sdwa v144, v21 dst_sel:DWORD dst_unused:UNUSED_PAD src0_sel:WORD_1
	v_cvt_f32_f16_sdwa v145, v20 dst_sel:DWORD dst_unused:UNUSED_PAD src0_sel:WORD_1
	v_cvt_f32_f16_sdwa v146, v19 dst_sel:DWORD dst_unused:UNUSED_PAD src0_sel:WORD_1
	v_cvt_f32_f16_e32 v148, v21
	v_cvt_f32_f16_e32 v149, v20
	v_cvt_f32_f16_e32 v150, v19
	v_lshlrev_b32_e32 v42, 1, v18
	global_load_dwordx4 v[18:21], v[26:27], off
	s_nop 0
	global_load_dwordx4 v[26:29], v[26:27], off offset:16
	s_add_i32 s3, s3, s85
	v_cvt_f32_f16_sdwa v130, v31 dst_sel:DWORD dst_unused:UNUSED_PAD src0_sel:WORD_1
	v_cvt_f32_f16_sdwa v131, v30 dst_sel:DWORD dst_unused:UNUSED_PAD src0_sel:WORD_1
	v_cvt_f32_f16_e32 v134, v31
	v_cvt_f32_f16_e32 v135, v30
	v_lshl_add_u64 v[30:31], v[64:65], 0, s[90:91]
	s_lshl_b32 s90, s14, 2
	s_lshl_b32 s3, s3, 6
	v_cvt_f32_f16_sdwa v122, v35 dst_sel:DWORD dst_unused:UNUSED_PAD src0_sel:WORD_1
	v_cvt_f32_f16_sdwa v123, v34 dst_sel:DWORD dst_unused:UNUSED_PAD src0_sel:WORD_1
	v_cvt_f32_f16_e32 v126, v35
	v_cvt_f32_f16_e32 v127, v34
	v_cvt_f32_f16_sdwa v128, v33 dst_sel:DWORD dst_unused:UNUSED_PAD src0_sel:WORD_1
	v_cvt_f32_f16_sdwa v129, v32 dst_sel:DWORD dst_unused:UNUSED_PAD src0_sel:WORD_1
	v_cvt_f32_f16_e32 v132, v33
	v_cvt_f32_f16_e32 v133, v32
	s_sub_i32 s9, s7, 32
	v_lshl_add_u64 v[32:33], v[66:67], 0, s[90:91]
	v_lshl_add_u64 v[34:35], s[86:87], 0, v[42:43]
	s_and_b32 s90, s3, 0xfc0
	v_add_co_u32_e32 v94, vcc, s33, v34
	v_lshl_add_u64 v[100:101], v[62:63], 0, s[90:91]
	s_and_b32 s90, s9, 0x7e0
	v_cvt_f32_f16_sdwa v106, v37 dst_sel:DWORD dst_unused:UNUSED_PAD src0_sel:WORD_1
	v_cvt_f32_f16_sdwa v107, v36 dst_sel:DWORD dst_unused:UNUSED_PAD src0_sel:WORD_1
	v_cvt_f32_f16_e32 v124, v37
	v_cvt_f32_f16_e32 v125, v36
	global_load_dwordx4 v[84:87], v42, s[86:87]
	global_load_dwordx4 v[88:91], v42, s[88:89]
	v_lshl_add_u64 v[36:37], s[88:89], 0, v[42:43]
	v_addc_co_u32_e32 v95, vcc, 0, v35, vcc
	v_or_b32_e32 v42, s90, v77
	v_add_co_u32_e32 v96, vcc, s33, v36
	v_lshlrev_b32_e32 v42, 1, v42
	s_add_i32 s8, s6, -3
	v_addc_co_u32_e32 v97, vcc, 0, v37, vcc
	v_lshl_add_u64 v[102:103], s[86:87], 0, v[42:43]
	s_min_u32 s0, s8, 59
	v_add_co_u32_e32 v102, vcc, s33, v102
	s_add_i32 s0, s0, s85
	v_lshl_add_u64 v[104:105], s[88:89], 0, v[42:43]
	v_addc_co_u32_e32 v103, vcc, 0, v103, vcc
	s_mov_b32 s15, s91
	s_lshl_b32 s0, s0, 6
	v_add_co_u32_e32 v120, vcc, s33, v104
	s_mov_b32 s11, s91
	v_lshl_add_u64 v[108:109], v[64:65], 0, s[14:15]
	s_lshl_b32 s14, s10, 6
	s_and_b32 s10, s0, 0xfc0
	v_addc_co_u32_e32 v121, vcc, 0, v105, vcc
	v_lshl_add_u64 v[92:93], v[62:63], 0, s[10:11]
	v_mov_b32_e32 v68, v43
	v_mov_b32_e32 v69, v43
	global_load_dwordx4 v[34:37], v[92:93], off
	s_nop 0
	global_load_dwordx4 v[92:95], v[94:95], off
	s_nop 0
	global_load_dwordx4 v[96:99], v[96:97], off
	s_and_b32 s2, s7, 0x7e0
	v_or_b32_e32 v152, s2, v77
	v_mov_b32_e32 v70, v43
	v_mov_b32_e32 v71, v43
	s_add_i32 s4, s4, s85
	s_mov_b32 s1, s91
	s_lshl_b32 s4, s4, 6
	s_lshl_b32 s0, s90, 2
	s_mov_b32 s5, s91
	s_and_b32 s4, s4, 0xfc0
	v_lshl_add_u64 v[114:115], v[66:67], 0, s[0:1]
	v_lshl_add_u64 v[110:111], v[62:63], 0, s[4:5]
	v_mov_b32_e32 v72, v43
	v_mov_b32_e32 v73, v43
	v_lshl_add_u64 v[112:113], v[64:65], 0, s[90:91]
	s_lshl_b32 s90, s2, 2
	s_waitcnt vmcnt(5) lgkmcnt(0)
	v_mul_f32_e32 v104, v18, v127
	v_mul_f32_e32 v105, v19, v123
	v_mul_f32_e32 v123, v20, v126
	v_mul_f32_e32 v122, v21, v122
	v_mul_f32_e32 v125, v125, v26
	v_mul_f32_e32 v107, v107, v27
	v_mul_f32_e32 v124, v124, v28
	v_mul_f32_e32 v106, v106, v29
	v_mul_f32_e32 v26, v83, v104
	v_mul_f32_e32 v27, v83, v105
	v_mul_f32_e32 v28, v83, v123
	v_mul_f32_e32 v29, v83, v122
	v_mul_f32_e32 v126, v83, v125
	v_mul_f32_e32 v127, v83, v107
	v_cvt_pk_bf16_f32 v18, v26, v27
	v_cvt_pk_bf16_f32 v19, v28, v29
	v_med3_f32 v26, v26, s82, v81
	v_med3_f32 v27, v27, s82, v81
	v_med3_f32 v156, v28, s82, v81
	v_med3_f32 v157, v29, s82, v81
	v_med3_f32 v28, v126, s82, v81
	v_med3_f32 v29, v127, s82, v81
	v_cvt_pk_fp8_f32 v68, v26, v27
	v_cvt_pk_fp8_f32 v69, v28, v29
	v_mul_f32_e32 v154, v83, v124
	v_mul_f32_e32 v155, v83, v106
	v_cvt_pk_bf16_f32 v20, v126, v127
	v_med3_f32 v126, v154, s82, v81
	v_med3_f32 v127, v155, s82, v81
	v_cvt_pk_bf16_f32 v21, v154, v155
	v_cvt_pk_fp8_f32 v68, v156, v157 op_sel:[0,0,1]
	v_mfma_f32_16x16x32_bf16 v[22:25], v[18:21], v[6:9], v[22:25]
	v_cvt_pk_fp8_f32 v69, v126, v127 op_sel:[0,0,1]
	v_lshlrev_b32_e32 v154, 16, v18
	v_and_b32_e32 v155, 0xffff0000, v18
	v_mfma_f32_16x16x32_bf16 v[26:29], v[18:21], v[2:5], v[38:41]
	v_lshlrev_b32_e32 v158, 16, v19
	v_and_b32_e32 v159, 0xffff0000, v19
	v_lshlrev_b32_e32 v160, 16, v20
	v_and_b32_e32 v161, 0xffff0000, v20
	v_lshlrev_b32_e32 v162, 16, v21
	v_and_b32_e32 v163, 0xffff0000, v21
	v_fma_f32 v38, v83, v104, -v154
	v_fma_f32 v39, v83, v105, -v155
	v_fma_f32 v40, v83, v123, -v158
	v_fma_f32 v41, v83, v122, -v159
	v_fma_f32 v104, v83, v125, -v160
	v_fma_f32 v105, v83, v107, -v161
	v_fma_f32 v107, v83, v124, -v162
	v_fma_f32 v106, v83, v106, -v163
	v_mfma_f32_16x16x32_bf16 v[10:13], v[18:21], v[10:13], v[22:25]
	global_store_dwordx2 v[30:31], v[68:69], off
	v_lshl_add_u64 v[116:117], v[66:67], 0, s[90:91]
	s_and_b32 s90, s14, 0xfc0
	v_mfma_f32_16x16x32_bf16 v[14:17], v[18:21], v[14:17], v[26:29]
	v_cvt_pk_bf16_f32 v18, v38, v39
	v_cvt_pk_bf16_f32 v19, v40, v41
	v_cvt_pk_bf16_f32 v20, v104, v105
	v_cvt_pk_bf16_f32 v21, v107, v106
	global_load_dwordx4 v[22:25], v[32:33], off
	s_nop 1
	global_load_dwordx4 v[26:29], v[32:33], off offset:16
	s_nop 0
	global_load_dwordx4 v[30:33], v[100:101], off
	global_load_dwordx4 v[38:41], v[102:103], off
	s_nop 0
	global_load_dwordx4 v[100:103], v42, s[88:89]
	v_mfma_f32_16x16x32_bf16 v[6:9], v[18:21], v[6:9], v[10:13]
	global_load_dwordx4 v[104:107], v42, s[86:87]
	s_nop 1
	global_load_dwordx4 v[10:13], v[120:121], off
	v_lshlrev_b32_e32 v42, 1, v152
	s_cmp_lt_u32 s6, 63
	v_mfma_f32_16x16x32_bf16 v[2:5], v[18:21], v[2:5], v[14:17]
	s_cselect_b64 s[0:1], -1, 0
	s_cmp_lg_u64 s[0:1], 0
	s_addc_u32 s0, s84, s6
	v_lshl_add_u64 v[14:15], s[86:87], 0, v[42:43]
	v_add_co_u32_e32 v68, vcc, s33, v14
	v_lshl_add_u64 v[16:17], s[88:89], 0, v[42:43]
	s_nop 0
	v_addc_co_u32_e32 v69, vcc, 0, v15, vcc
	v_add_co_u32_e32 v120, vcc, s33, v16
	s_lshl_b32 s0, s0, 5
	s_nop 0
	v_addc_co_u32_e32 v121, vcc, 0, v17, vcc
	s_and_b32 s0, s0, 0x7e0
	v_or_b32_e32 v153, s0, v77
	v_lshl_add_u64 v[118:119], v[62:63], 0, s[90:91]
	s_mov_b32 s3, s91
	s_add_i32 s6, s6, 4
	s_addk_i32 s7, 0x80
	s_cmp_gt_u32 s8, 59
	s_waitcnt vmcnt(5) lgkmcnt(0)
; __device__ __forceinline__ void p7_ffn_prep(const Ctx& C, bool dummy = false) {
;     ...
;           for (int d = 0; d < 4; ++d) { const int cl = c4 + d, c = P7_RC(cl);
;             const f32x8 xf = __builtin_convertvector(xq[d], f32x8); const f32x4 xa = {xf[0], xf[1], xf[2], xf[3]}, xb = {xf[4], xf[5], xf[6], xf[7]}, ga = *(const f32x4*)(fg + 32 * c), gb = *(const f32x4*)(fg + 32 * c + 4);
;             const bf16x8 b0h = b0hN, b1h = b1hN, b0l = b0lN, b1l = b1lN;
;             { const int cx = P7_RC(cl + 4 < 64 ? cl + 4 : 63); xq[d] = *(const f16x8*)(x1 + 32 * cx);
;               const int cn = P7_RC(cl < 63 ? cl + 1 : cl); const size_t bn = (size_t)i * D_ + 32 * cn + 8 * g4;
;               b0hN = *(const bf16x8*)(WRH + bn); b1hN = *(const bf16x8*)(WRH + bn + (size_t)16 * D_); b0lN = *(const bf16x8*)(WRL + bn); b1lN = *(const bf16x8*)(WRL + bn + (size_t)16 * D_); }
;             float h[8]; h[0] = xa[0] * ga[0] * rstd; h[1] = xa[1] * ga[1] * rstd; h[2] = xa[2] * ga[2] * rstd; h[3] = xa[3] * ga[3] * rstd; h[4] = xb[0] * gb[0] * rstd; h[5] = xb[1] * gb[1] * rstd; h[6] = xb[2] * gb[2] * rstd; h[7] = xb[3] * gb[3] * rstd;
;             u32x4 hi; hi.x = cvt_pk_bf16(h[0], h[1]); hi.y = cvt_pk_bf16(h[2], h[3]); hi.z = cvt_pk_bf16(h[4], h[5]); hi.w = cvt_pk_bf16(h[6], h[7]);
;             { u32x2 w8; w8.x = pk4_fp8(h[0], h[1], h[2], h[3]); w8.y = pk4_fp8(h[4], h[5], h[6], h[7]); *(u32x2*)(h2 + 32 * c) = w8; }
;             u32x4 lo; lo.x = cvt_pk_bf16(h[0] - __uint_as_float(hi.x << 16), h[1] - __uint_as_float(hi.x & 0xFFFF0000u)); lo.y = cvt_pk_bf16(h[2] - __uint_as_float(hi.y << 16), h[3] - __uint_as_float(hi.y & 0xFFFF0000u));
;             lo.z = cvt_pk_bf16(h[4] - __uint_as_float(hi.z << 16), h[5] - __uint_as_float(hi.z & 0xFFFF0000u)); lo.w = cvt_pk_bf16(h[6] - __uint_as_float(hi.w << 16), h[7] - __uint_as_float(hi.w & 0xFFFF0000u));
;             const bf16x8 ah = __builtin_bit_cast(bf16x8, hi), al = __builtin_bit_cast(bf16x8, lo);
;             a0 = __builtin_amdgcn_mfma_f32_16x16x32_bf16(ah, b0h, a0, 0, 0, 0); a0 = __builtin_amdgcn_mfma_f32_16x16x32_bf16(ah, b0l, a0, 0, 0, 0); a0 = __builtin_amdgcn_mfma_f32_16x16x32_bf16(al, b0h, a0, 0, 0, 0);
;             a1 = __builtin_amdgcn_mfma_f32_16x16x32_bf16(ah, b1h, a1, 0, 0, 0); a1 = __builtin_amdgcn_mfma_f32_16x16x32_bf16(ah, b1l, a1, 0, 0, 0); a1 = __builtin_amdgcn_mfma_f32_16x16x32_bf16(al, b1h, a1, 0, 0, 0);
	v_mul_f32_e32 v18, v135, v22
	v_mul_f32_e32 v19, v131, v23
	v_mul_f32_e32 v22, v133, v26
	v_mul_f32_e32 v23, v129, v27
	v_mul_f32_e32 v20, v134, v24
	v_mul_f32_e32 v21, v130, v25
	v_mul_f32_e32 v26, v83, v18
	v_mul_f32_e32 v27, v83, v19
	v_mul_f32_e32 v122, v83, v22
	v_mul_f32_e32 v123, v83, v23
	v_mul_f32_e32 v24, v132, v28
	v_mul_f32_e32 v25, v128, v29
	v_mul_f32_e32 v28, v83, v20
	v_mul_f32_e32 v29, v83, v21
	v_cvt_pk_bf16_f32 v14, v26, v27
	v_cvt_pk_bf16_f32 v15, v28, v29
	v_cvt_pk_bf16_f32 v16, v122, v123
	v_med3_f32 v26, v26, s82, v81
	v_med3_f32 v27, v27, s82, v81
	v_med3_f32 v122, v122, s82, v81
	v_med3_f32 v123, v123, s82, v81
	v_cvt_pk_fp8_f32 v70, v26, v27
	v_cvt_pk_fp8_f32 v71, v122, v123
	v_mul_f32_e32 v124, v83, v24
	v_mul_f32_e32 v125, v83, v25
	v_cvt_pk_bf16_f32 v17, v124, v125
	v_med3_f32 v28, v28, s82, v81
	v_med3_f32 v29, v29, s82, v81
	v_med3_f32 v124, v124, s82, v81
	v_med3_f32 v125, v125, s82, v81
	v_mfma_f32_16x16x32_bf16 v[6:9], v[14:17], v[84:87], v[6:9]
	v_cvt_pk_fp8_f32 v70, v28, v29 op_sel:[0,0,1]
	v_cvt_pk_fp8_f32 v71, v124, v125 op_sel:[0,0,1]
	v_lshlrev_b32_e32 v26, 16, v14
	v_mfma_f32_16x16x32_bf16 v[2:5], v[14:17], v[92:95], v[2:5]
	v_and_b32_e32 v27, 0xffff0000, v14
	v_lshlrev_b32_e32 v122, 16, v15
	v_and_b32_e32 v123, 0xffff0000, v15
	v_lshlrev_b32_e32 v126, 16, v16
	v_and_b32_e32 v127, 0xffff0000, v16
	v_lshlrev_b32_e32 v128, 16, v17
	v_and_b32_e32 v129, 0xffff0000, v17
	v_fma_f32 v18, v83, v18, -v26
	v_fma_f32 v19, v83, v19, -v27
	v_fma_f32 v20, v83, v20, -v122
	v_fma_f32 v21, v83, v21, -v123
	v_fma_f32 v22, v83, v22, -v126
	v_fma_f32 v23, v83, v23, -v127
	v_fma_f32 v24, v83, v24, -v128
	v_fma_f32 v25, v83, v25, -v129
	v_mfma_f32_16x16x32_bf16 v[6:9], v[14:17], v[88:91], v[6:9]
	global_store_dwordx2 v[108:109], v[70:71], off
	v_mfma_f32_16x16x32_bf16 v[2:5], v[14:17], v[96:99], v[2:5]
	v_cvt_pk_bf16_f32 v14, v18, v19
	v_cvt_pk_bf16_f32 v15, v20, v21
	v_cvt_pk_bf16_f32 v16, v22, v23
	v_cvt_pk_bf16_f32 v17, v24, v25
	global_load_dwordx4 v[18:21], v[114:115], off
	global_load_dwordx4 v[22:25], v[114:115], off offset:16
	global_load_dwordx4 v[26:29], v[110:111], off
	s_nop 0
	global_load_dwordx4 v[68:71], v[68:69], off
	s_nop 0
	global_load_dwordx4 v[88:91], v42, s[88:89]
	v_mfma_f32_16x16x32_bf16 v[2:5], v[14:17], v[92:95], v[2:5]
	s_waitcnt vmcnt(3) lgkmcnt(0)
	v_mul_f32_e32 v18, v143, v18
	v_mul_f32_e32 v19, v139, v19
	v_mul_f32_e32 v22, v141, v22
	v_mul_f32_e32 v23, v137, v23
	v_mul_f32_e32 v20, v142, v20
	v_mul_f32_e32 v21, v138, v21
	v_mul_f32_e32 v92, v83, v18
	v_mul_f32_e32 v93, v83, v19
	v_mul_f32_e32 v108, v83, v22
	v_mul_f32_e32 v109, v83, v23
	v_mfma_f32_16x16x32_bf16 v[6:9], v[14:17], v[84:87], v[6:9]
	global_load_dwordx4 v[84:87], v42, s[86:87]
	global_load_dwordx4 v[96:99], v[120:121], off
	v_mul_f32_e32 v94, v83, v20
	v_mul_f32_e32 v95, v83, v21
	v_cvt_pk_bf16_f32 v14, v92, v93
	v_cvt_pk_bf16_f32 v15, v94, v95
	v_cvt_pk_bf16_f32 v16, v108, v109
	v_med3_f32 v92, v92, s82, v81
	v_med3_f32 v93, v93, s82, v81
	v_med3_f32 v108, v108, s82, v81
	v_med3_f32 v109, v109, s82, v81
	v_cvt_pk_fp8_f32 v72, v92, v93
	v_cvt_pk_fp8_f32 v73, v108, v109
	v_mul_f32_e32 v24, v140, v24
	v_mul_f32_e32 v25, v136, v25
	v_mul_f32_e32 v110, v83, v24
	v_mul_f32_e32 v111, v83, v25
	v_cvt_pk_bf16_f32 v17, v110, v111
	v_med3_f32 v94, v94, s82, v81
	v_med3_f32 v95, v95, s82, v81
	v_med3_f32 v110, v110, s82, v81
	v_med3_f32 v111, v111, s82, v81
	v_cvt_pk_fp8_f32 v72, v94, v95 op_sel:[0,0,1]
	v_cvt_pk_fp8_f32 v73, v110, v111 op_sel:[0,0,1]
	v_lshlrev_b32_e32 v92, 16, v14
	v_and_b32_e32 v93, 0xffff0000, v14
	v_lshlrev_b32_e32 v108, 16, v15
	v_lshlrev_b32_e32 v122, 16, v16
	v_and_b32_e32 v123, 0xffff0000, v16
	v_lshlrev_b32_e32 v124, 16, v17
	v_and_b32_e32 v125, 0xffff0000, v17
	v_and_b32_e32 v109, 0xffff0000, v15
	v_fma_f32 v18, v83, v18, -v92
	v_fma_f32 v19, v83, v19, -v93
	v_fma_f32 v20, v83, v20, -v108
	v_fma_f32 v92, v83, v22, -v122
	v_fma_f32 v93, v83, v23, -v123
	v_fma_f32 v108, v83, v24, -v124
	v_fma_f32 v25, v83, v25, -v125
	v_fma_f32 v21, v83, v21, -v109
	global_store_dwordx2 v[112:113], v[72:73], off
	v_cvt_pk_bf16_f32 v22, v18, v19
	v_cvt_pk_bf16_f32 v23, v20, v21
	v_cvt_pk_bf16_f32 v24, v92, v93
	v_cvt_pk_bf16_f32 v25, v108, v25
	global_load_dwordx4 v[92:95], v[116:117], off
	global_load_dwordx4 v[108:111], v[116:117], off offset:16
	v_lshlrev_b32_e32 v42, 1, v153
	v_lshl_add_u64 v[114:115], s[86:87], 0, v[42:43]
	v_mfma_f32_16x16x32_bf16 v[6:9], v[14:17], v[104:107], v[6:9]
	v_add_co_u32_e32 v72, vcc, s33, v114
	v_lshl_add_u64 v[120:121], s[88:89], 0, v[42:43]
	v_mfma_f32_16x16x32_bf16 v[2:5], v[14:17], v[38:41], v[2:5]
	v_addc_co_u32_e32 v73, vcc, 0, v115, vcc
	v_add_co_u32_e32 v116, vcc, s33, v120
	v_mfma_f32_16x16x32_bf16 v[100:103], v[14:17], v[100:103], v[6:9]
	s_nop 0
	v_addc_co_u32_e32 v117, vcc, 0, v121, vcc
	s_waitcnt vmcnt(0) lgkmcnt(0)
; __device__ __forceinline__ void p7_ffn_prep(const Ctx& C, bool dummy = false) {
;     ...
;             const f32x8 xf = __builtin_convertvector(xq[d], f32x8); const f32x4 xa = {xf[0], xf[1], xf[2], xf[3]}, xb = {xf[4], xf[5], xf[6], xf[7]}, ga = *(const f32x4*)(fg + 32 * c), gb = *(const f32x4*)(fg + 32 * c + 4);
;             const bf16x8 b0h = b0hN, b1h = b1hN, b0l = b0lN, b1l = b1lN;
;             { const int cx = P7_RC(cl + 4 < 64 ? cl + 4 : 63); xq[d] = *(const f16x8*)(x1 + 32 * cx);
;               const int cn = P7_RC(cl < 63 ? cl + 1 : cl); const size_t bn = (size_t)i * D_ + 32 * cn + 8 * g4;
;               b0hN = *(const bf16x8*)(WRH + bn); b1hN = *(const bf16x8*)(WRH + bn + (size_t)16 * D_); b0lN = *(const bf16x8*)(WRL + bn); b1lN = *(const bf16x8*)(WRL + bn + (size_t)16 * D_); }
;             float h[8]; h[0] = xa[0] * ga[0] * rstd; h[1] = xa[1] * ga[1] * rstd; h[2] = xa[2] * ga[2] * rstd; h[3] = xa[3] * ga[3] * rstd; h[4] = xb[0] * gb[0] * rstd; h[5] = xb[1] * gb[1] * rstd; h[6] = xb[2] * gb[2] * rstd; h[7] = xb[3] * gb[3] * rstd;
;             u32x4 hi; hi.x = cvt_pk_bf16(h[0], h[1]); hi.y = cvt_pk_bf16(h[2], h[3]); hi.z = cvt_pk_bf16(h[4], h[5]); hi.w = cvt_pk_bf16(h[6], h[7]);
;             { u32x2 w8; w8.x = pk4_fp8(h[0], h[1], h[2], h[3]); w8.y = pk4_fp8(h[4], h[5], h[6], h[7]); *(u32x2*)(h2 + 32 * c) = w8; }
;             u32x4 lo; lo.x = cvt_pk_bf16(h[0] - __uint_as_float(hi.x << 16), h[1] - __uint_as_float(hi.x & 0xFFFF0000u)); lo.y = cvt_pk_bf16(h[2] - __uint_as_float(hi.y << 16), h[3] - __uint_as_float(hi.y & 0xFFFF0000u));
;             lo.z = cvt_pk_bf16(h[4] - __uint_as_float(hi.z << 16), h[5] - __uint_as_float(hi.z & 0xFFFF0000u)); lo.w = cvt_pk_bf16(h[6] - __uint_as_float(hi.w << 16), h[7] - __uint_as_float(hi.w & 0xFFFF0000u));
;             const bf16x8 ah = __builtin_bit_cast(bf16x8, hi), al = __builtin_bit_cast(bf16x8, lo);
;             a0 = __builtin_amdgcn_mfma_f32_16x16x32_bf16(ah, b0h, a0, 0, 0, 0); a0 = __builtin_amdgcn_mfma_f32_16x16x32_bf16(ah, b0l, a0, 0, 0, 0); a0 = __builtin_amdgcn_mfma_f32_16x16x32_bf16(al, b0h, a0, 0, 0, 0);
;             a1 = __builtin_amdgcn_mfma_f32_16x16x32_bf16(ah, b1h, a1, 0, 0, 0); a1 = __builtin_amdgcn_mfma_f32_16x16x32_bf16(ah, b1l, a1, 0, 0, 0); a1 = __builtin_amdgcn_mfma_f32_16x16x32_bf16(al, b1h, a1, 0, 0, 0);
	v_mul_f32_e32 v108, v149, v108
	v_mfma_f32_16x16x32_bf16 v[112:115], v[14:17], v[10:13], v[2:5]
	global_load_dwordx4 v[18:21], v[118:119], off
	s_nop 1
	global_load_dwordx4 v[2:5], v[72:73], off
	global_load_dwordx4 v[10:13], v42, s[88:89]
	global_load_dwordx4 v[6:9], v42, s[86:87]
	global_load_dwordx4 v[14:17], v[116:117], off
	v_mul_f32_e32 v42, v151, v92
	v_mul_f32_e32 v109, v145, v109
	v_mfma_f32_16x16x32_bf16 v[100:103], v[22:25], v[104:107], v[100:103]
	v_mul_f32_e32 v106, v147, v93
	v_mul_f32_e32 v107, v150, v94
	v_mul_f32_e32 v92, v83, v42
	v_mfma_f32_16x16x32_bf16 v[22:25], v[22:25], v[38:41], v[112:115]
	v_mul_f32_e32 v93, v83, v106
	v_mul_f32_e32 v94, v83, v107
	v_mov_b32_e32 v72, v43
	v_mul_f32_e32 v112, v146, v95
	v_mul_f32_e32 v95, v83, v112
	v_mul_f32_e32 v113, v83, v108
	v_mul_f32_e32 v114, v83, v109
	v_mov_b32_e32 v73, v43
	v_mul_f32_e32 v110, v148, v110
	v_mul_f32_e32 v111, v144, v111
	v_cvt_pk_bf16_f32 v38, v92, v93
	v_cvt_pk_bf16_f32 v39, v94, v95
	v_med3_f32 v92, v92, s82, v81
	v_med3_f32 v93, v93, s82, v81
	v_med3_f32 v117, v94, s82, v81
	v_med3_f32 v118, v95, s82, v81
	v_med3_f32 v94, v113, s82, v81
	v_med3_f32 v95, v114, s82, v81
	v_mul_f32_e32 v115, v83, v110
	v_mul_f32_e32 v116, v83, v111
	v_cvt_pk_bf16_f32 v40, v113, v114
	v_cvt_pk_bf16_f32 v41, v115, v116
	v_cvt_pk_fp8_f32 v72, v92, v93
	v_cvt_pk_fp8_f32 v73, v94, v95
	v_mfma_f32_16x16x32_bf16 v[92:95], v[38:41], v[84:87], v[100:103]
	v_med3_f32 v113, v115, s82, v81
	v_med3_f32 v114, v116, s82, v81
	v_lshlrev_b32_e32 v115, 16, v38
	v_mfma_f32_16x16x32_bf16 v[22:25], v[38:41], v[68:71], v[22:25]
	v_and_b32_e32 v116, 0xffff0000, v38
	v_lshlrev_b32_e32 v119, 16, v39
	v_and_b32_e32 v120, 0xffff0000, v39
	v_lshlrev_b32_e32 v121, 16, v40
	v_and_b32_e32 v100, 0xffff0000, v40
	v_lshlrev_b32_e32 v101, 16, v41
	v_and_b32_e32 v102, 0xffff0000, v41
	v_cvt_pk_fp8_f32 v72, v117, v118 op_sel:[0,0,1]
	v_mfma_f32_16x16x32_bf16 v[88:91], v[38:41], v[88:91], v[92:95]
	v_cvt_pk_fp8_f32 v73, v113, v114 op_sel:[0,0,1]
	v_lshl_add_u64 v[104:105], v[64:65], 0, s[2:3]
	v_fma_f32 v42, v83, v42, -v115
	v_mfma_f32_16x16x32_bf16 v[38:41], v[38:41], v[96:99], v[22:25]
	v_fma_f32 v103, v83, v106, -v116
	v_fma_f32 v106, v83, v107, -v119
	v_fma_f32 v107, v83, v112, -v120
	v_fma_f32 v108, v83, v108, -v121
	v_fma_f32 v100, v83, v109, -v100
	v_fma_f32 v101, v83, v110, -v101
	v_fma_f32 v102, v83, v111, -v102
	global_store_dwordx2 v[104:105], v[72:73], off
	v_cvt_pk_bf16_f32 v92, v42, v103
	v_cvt_pk_bf16_f32 v93, v106, v107
	v_cvt_pk_bf16_f32 v94, v108, v100
	v_cvt_pk_bf16_f32 v95, v101, v102
	s_nop 0
	v_mfma_f32_16x16x32_bf16 v[22:25], v[92:95], v[84:87], v[88:91]
	v_mfma_f32_16x16x32_bf16 v[38:41], v[92:95], v[68:71], v[38:41]
	s_cbranch_scc0 .LBB0_899
	s_waitcnt vmcnt(4)
	v_add_u32_e32 v2, 0x400, v74
	s_nop 4
	ds_write2_b32 v2, v22, v38 offset1:16
	ds_write2_b32 v2, v23, v39 offset0:33 offset1:49
	ds_write2_b32 v2, v24, v40 offset0:66 offset1:82
	ds_write2_b32 v2, v25, v41 offset0:99 offset1:115
	s_waitcnt vmcnt(3)
	v_mov_b32_e32 v12, 0
	v_mov_b32_e32 v20, 0
	v_mov_b32_e32 v18, 0
	s_waitcnt vmcnt(1)
	v_mov_b32_e32 v16, 0
	v_mov_b32_e32 v14, 0
	v_mov_b32_e32 v10, 0
	v_mov_b32_e32 v11, 0
	v_mov_b32_e32 v13, 0
	v_mov_b32_e32 v2, 0
	v_mov_b32_e32 v4, 0
	v_mov_b32_e32 v6, 0
	v_mov_b32_e32 v8, 0
	s_mov_b64 s[2:3], exec
	v_readlane_b32 s0, v254, 22
	v_readlane_b32 s1, v254, 23
	v_writelane_b32 v254, s2, 30
	s_and_b64 s[0:1], s[2:3], s[0:1]
	s_nop 0
	v_writelane_b32 v254, s3, 31
	s_mov_b64 exec, s[0:1]
	s_cbranch_execz .LBB0_902
	v_readlane_b32 s0, v254, 15
	v_readlane_b32 s1, v254, 16
	v_add_u32_e32 v4, 0x400, v79
	ds_read2_b32 v[8:9], v4 offset1:1
	v_mov_b64_e32 v[2:3], s[0:1]
	flat_load_dwordx2 v[2:3], v[2:3] offset:176
	s_mov_b32 s0, 0xff800000
	s_waitcnt vmcnt(0) lgkmcnt(0)
	flat_load_dwordx4 v[4:7], v[2:3]
	flat_load_dwordx4 v[16:19], v[2:3] offset:16
	flat_load_dwordx4 v[20:23], v[2:3] offset:32
	flat_load_dwordx4 v[24:27], v[2:3] offset:48
	flat_load_dwordx4 v[28:31], v[2:3] offset:64
	flat_load_dwordx4 v[32:35], v[2:3] offset:80
	s_waitcnt vmcnt(0) lgkmcnt(0)
	v_add_f32_e32 v11, v8, v4
	v_add_u32_e32 v4, 0x408, v79
	v_add_f32_e32 v9, v9, v5
	ds_read2_b32 v[4:5], v4 offset1:1
	v_cmp_lg_f32_e32 vcc, s0, v11
	v_cmp_nlg_f32_e64 s[10:11], s0, v11
	s_waitcnt lgkmcnt(0)
	v_add_f32_e32 v8, v4, v6
	v_add_u32_e32 v4, 0x410, v79
	v_add_f32_e32 v7, v5, v7
	ds_read2_b32 v[4:5], v4 offset1:1
	s_waitcnt lgkmcnt(0)
	v_add_f32_e32 v15, v4, v16
	v_add_u32_e32 v4, 0x418, v79
	v_add_f32_e32 v13, v5, v17
	ds_read2_b32 v[4:5], v4 offset1:1
	s_waitcnt lgkmcnt(0)
	v_add_f32_e32 v12, v4, v18
	v_add_u32_e32 v4, 0x420, v79
	v_add_f32_e32 v10, v5, v19
	ds_read2_b32 v[4:5], v4 offset1:1
	s_waitcnt lgkmcnt(0)
	v_add_f32_e32 v19, v4, v20
	v_add_u32_e32 v4, 0x428, v79
	v_add_f32_e32 v17, v5, v21
	ds_read2_b32 v[4:5], v4 offset1:1
	s_waitcnt lgkmcnt(0)
	v_add_f32_e32 v16, v4, v22
	v_add_u32_e32 v4, 0x430, v79
	v_add_f32_e32 v14, v5, v23
	ds_read2_b32 v[4:5], v4 offset1:1
	s_waitcnt lgkmcnt(0)
	v_add_f32_e32 v23, v4, v24
	v_add_u32_e32 v4, 0x438, v79
	v_add_f32_e32 v21, v5, v25
	ds_read2_b32 v[4:5], v4 offset1:1
	s_waitcnt lgkmcnt(0)
	v_add_f32_e32 v20, v4, v26
	v_add_u32_e32 v4, 0x440, v79
	v_add_f32_e32 v18, v5, v27
	ds_read2_b32 v[4:5], v4 offset1:1
	s_waitcnt lgkmcnt(0)
	v_add_f32_e32 v27, v4, v28
	v_add_u32_e32 v4, 0x448, v79
	v_add_f32_e32 v25, v5, v29
	ds_read2_b32 v[4:5], v4 offset1:1
	s_waitcnt lgkmcnt(0)
	v_add_f32_e32 v24, v4, v30
	v_add_u32_e32 v4, 0x450, v79
	v_add_f32_e32 v22, v5, v31
	ds_read2_b32 v[4:5], v4 offset1:1
	s_waitcnt lgkmcnt(0)
; __device__ __forceinline__ void p7_ffn_prep(const Ctx& C, bool dummy = false) {
;     ...
;             for (int e = 0; e < 32; ++e) v[e] = lg[lane * 33 + e] + C.ka->in[I_BR][e];
;             float tv[4];
; #pragma unroll
;             for (int k = 0; k < 4; ++k) { float best = -__builtin_inff(); int be = 0;
; #pragma unroll
;                 for (int e = 0; e < 32; ++e) { const bool taken = (k > 0 && e == e4[0]) || (k > 1 && e == e4[1]) || (k > 2 && e == e4[2]); if (!taken && v[e] > best) { best = v[e]; be = e; } }
;                 e4[k] = be; tv[k] = best; }
	v_add_f32_e32 v31, v4, v32
	v_add_u32_e32 v4, 0x458, v79
	v_add_f32_e32 v29, v5, v33
	ds_read2_b32 v[4:5], v4 offset1:1
	s_waitcnt lgkmcnt(0)
	v_add_f32_e32 v28, v4, v34
	v_add_f32_e32 v26, v5, v35
	flat_load_dwordx4 v[34:37], v[2:3] offset:96
	v_add_u32_e32 v4, 0x460, v79
	ds_read2_b32 v[4:5], v4 offset1:1
	s_waitcnt vmcnt(0) lgkmcnt(0)
	v_add_f32_e32 v34, v4, v34
	v_add_u32_e32 v4, 0x468, v79
	v_add_f32_e32 v33, v5, v35
	ds_read2_b32 v[4:5], v4 offset1:1
	s_waitcnt lgkmcnt(0)
	v_add_f32_e32 v32, v4, v36
	v_add_u32_e32 v4, 0x470, v79
	v_add_f32_e32 v30, v5, v37
	ds_read2_b32 v[36:37], v4 offset1:1
	flat_load_dwordx4 v[2:5], v[2:3] offset:112
	s_waitcnt vmcnt(0) lgkmcnt(0)
	v_add_f32_e32 v35, v36, v2
	v_add_u32_e32 v2, 0x478, v79
	v_add_f32_e32 v3, v37, v3
	ds_read2_b32 v[36:37], v2 offset1:1
	v_cndmask_b32_e32 v2, v82, v11, vcc
	v_cmp_gt_f32_e32 vcc, v9, v2
	s_waitcnt lgkmcnt(0)
	v_add_f32_e32 v36, v36, v4
	v_cndmask_b32_e32 v2, v2, v9, vcc
	v_cndmask_b32_e64 v4, 0, 1, vcc
	v_cmp_gt_f32_e32 vcc, v8, v2
	v_add_f32_e32 v5, v37, v5
	s_nop 0
	v_cndmask_b32_e32 v2, v2, v8, vcc
	v_cndmask_b32_e64 v4, v4, 2, vcc
	v_cmp_gt_f32_e32 vcc, v7, v2
	s_nop 1
	v_cndmask_b32_e32 v2, v2, v7, vcc
	v_cndmask_b32_e64 v4, v4, 3, vcc
	v_cmp_gt_f32_e32 vcc, v15, v2
	s_nop 1
	v_cndmask_b32_e32 v2, v2, v15, vcc
	v_cndmask_b32_e64 v4, v4, 4, vcc
	v_cmp_gt_f32_e32 vcc, v13, v2
	s_nop 1
	v_cndmask_b32_e32 v2, v2, v13, vcc
	v_cndmask_b32_e64 v4, v4, 5, vcc
	v_cmp_gt_f32_e32 vcc, v12, v2
	s_nop 1
	v_cndmask_b32_e32 v2, v2, v12, vcc
	v_cndmask_b32_e64 v4, v4, 6, vcc
	v_cmp_gt_f32_e32 vcc, v10, v2
	s_nop 1
	v_cndmask_b32_e32 v2, v2, v10, vcc
	v_cndmask_b32_e64 v4, v4, 7, vcc
	v_cmp_gt_f32_e32 vcc, v19, v2
	s_nop 1
	v_cndmask_b32_e32 v2, v2, v19, vcc
	v_cndmask_b32_e64 v4, v4, 8, vcc
	v_cmp_gt_f32_e32 vcc, v17, v2
	s_nop 1
	v_cndmask_b32_e32 v2, v2, v17, vcc
	v_cndmask_b32_e64 v4, v4, 9, vcc
	v_cmp_gt_f32_e32 vcc, v16, v2
	s_nop 1
	v_cndmask_b32_e32 v2, v2, v16, vcc
	v_cndmask_b32_e64 v4, v4, 10, vcc
	v_cmp_gt_f32_e32 vcc, v14, v2
	s_nop 1
	v_cndmask_b32_e32 v2, v2, v14, vcc
	v_cndmask_b32_e64 v4, v4, 11, vcc
	v_cmp_gt_f32_e32 vcc, v23, v2
	s_nop 1
	v_cndmask_b32_e32 v2, v2, v23, vcc
	v_cndmask_b32_e64 v4, v4, 12, vcc
	v_cmp_gt_f32_e32 vcc, v21, v2
	s_nop 1
	v_cndmask_b32_e32 v2, v2, v21, vcc
	v_cndmask_b32_e64 v4, v4, 13, vcc
	v_cmp_gt_f32_e32 vcc, v20, v2
	s_nop 1
	v_cndmask_b32_e32 v2, v2, v20, vcc
	v_cndmask_b32_e64 v4, v4, 14, vcc
	v_cmp_gt_f32_e32 vcc, v18, v2
	s_nop 1
	v_cndmask_b32_e32 v2, v2, v18, vcc
	v_cndmask_b32_e64 v4, v4, 15, vcc
	v_cmp_gt_f32_e32 vcc, v27, v2
	s_nop 1
	v_cndmask_b32_e32 v2, v2, v27, vcc
	v_cndmask_b32_e64 v4, v4, 16, vcc
	v_cmp_gt_f32_e32 vcc, v25, v2
	s_nop 1
	v_cndmask_b32_e32 v2, v2, v25, vcc
	v_cndmask_b32_e64 v4, v4, 17, vcc
	v_cmp_gt_f32_e32 vcc, v24, v2
	s_nop 1
	v_cndmask_b32_e32 v2, v2, v24, vcc
	v_cndmask_b32_e64 v4, v4, 18, vcc
	v_cmp_gt_f32_e32 vcc, v22, v2
	s_nop 1
	v_cndmask_b32_e32 v2, v2, v22, vcc
	v_cndmask_b32_e64 v4, v4, 19, vcc
	v_cmp_gt_f32_e32 vcc, v31, v2
	s_nop 1
	v_cndmask_b32_e32 v2, v2, v31, vcc
	v_cndmask_b32_e64 v4, v4, 20, vcc
	v_cmp_gt_f32_e32 vcc, v29, v2
	s_nop 1
	v_cndmask_b32_e32 v2, v2, v29, vcc
	v_cndmask_b32_e64 v4, v4, 21, vcc
	v_cmp_gt_f32_e32 vcc, v28, v2
	s_nop 1
	v_cndmask_b32_e32 v2, v2, v28, vcc
	v_cndmask_b32_e64 v4, v4, 22, vcc
	v_cmp_gt_f32_e32 vcc, v26, v2
	s_nop 1
	v_cndmask_b32_e32 v2, v2, v26, vcc
	v_cndmask_b32_e64 v4, v4, 23, vcc
	v_cmp_gt_f32_e32 vcc, v34, v2
	s_nop 1
	v_cndmask_b32_e32 v2, v2, v34, vcc
	v_cndmask_b32_e64 v4, v4, 24, vcc
	v_cmp_gt_f32_e32 vcc, v33, v2
	s_nop 1
	v_cndmask_b32_e32 v2, v2, v33, vcc
	v_cndmask_b32_e64 v4, v4, 25, vcc
	v_cmp_gt_f32_e32 vcc, v32, v2
	s_nop 1
	v_cndmask_b32_e32 v2, v2, v32, vcc
	v_cndmask_b32_e64 v4, v4, 26, vcc
	v_cmp_gt_f32_e32 vcc, v30, v2
	s_nop 1
	v_cndmask_b32_e32 v2, v2, v30, vcc
	v_cndmask_b32_e64 v4, v4, 27, vcc
	v_cmp_gt_f32_e32 vcc, v35, v2
	s_nop 1
	v_cndmask_b32_e32 v2, v2, v35, vcc
	v_cndmask_b32_e64 v4, v4, 28, vcc
	v_cmp_gt_f32_e32 vcc, v3, v2
	s_nop 1
	v_cndmask_b32_e32 v2, v2, v3, vcc
	v_cndmask_b32_e64 v4, v4, 29, vcc
	v_cmp_gt_f32_e32 vcc, v36, v2
	s_nop 1
	v_cndmask_b32_e32 v2, v2, v36, vcc
	v_cndmask_b32_e64 v4, v4, 30, vcc
	v_cmp_gt_f32_e32 vcc, v5, v2
	s_nop 1
	v_cndmask_b32_e32 v37, v2, v5, vcc
	v_cndmask_b32_e64 v2, v4, 31, vcc
	v_cmp_eq_u32_e32 vcc, 0, v2
	s_or_b64 vcc, vcc, s[10:11]
	v_cmp_eq_u32_e64 s[10:11], 1, v2
	v_cndmask_b32_e32 v4, v11, v82, vcc
	v_cmp_ngt_f32_e64 s[12:13], v9, v4
	s_or_b64 s[12:13], s[10:11], s[12:13]
	s_xor_b64 s[0:1], s[12:13], -1
	v_cndmask_b32_e64 v4, v9, v4, s[12:13]
	v_cndmask_b32_e64 v6, 0, 1, s[0:1]
	v_cmp_eq_u32_e64 s[0:1], 2, v2
	v_cmp_ngt_f32_e64 s[14:15], v8, v4
	s_or_b64 s[14:15], s[0:1], s[14:15]
	v_cmp_eq_u32_e64 s[2:3], 3, v2
	v_cndmask_b32_e64 v4, v8, v4, s[14:15]
	v_cmp_ngt_f32_e64 s[16:17], v7, v4
	s_or_b64 s[16:17], s[2:3], s[16:17]
	v_cndmask_b32_e64 v6, 2, v6, s[14:15]
	v_cndmask_b32_e64 v4, v7, v4, s[16:17]
	v_cndmask_b32_e64 v6, 3, v6, s[16:17]
	v_cmp_eq_u32_e64 s[16:17], 4, v2
	v_cmp_ngt_f32_e64 s[18:19], v15, v4
	s_or_b64 s[18:19], s[16:17], s[18:19]
	v_cmp_eq_u32_e64 s[72:73], 29, v2
	v_cndmask_b32_e64 v4, v15, v4, s[18:19]
	v_cndmask_b32_e64 v6, 4, v6, s[18:19]
	v_cmp_eq_u32_e64 s[18:19], 5, v2
	v_cmp_ngt_f32_e64 s[20:21], v13, v4
	s_or_b64 s[20:21], s[18:19], s[20:21]
	v_cmp_eq_u32_e64 s[70:71], 30, v2
	v_cndmask_b32_e64 v4, v13, v4, s[20:21]
	v_cndmask_b32_e64 v6, 5, v6, s[20:21]
	v_cmp_eq_u32_e64 s[20:21], 6, v2
	v_cmp_ngt_f32_e64 s[22:23], v12, v4
	s_or_b64 s[22:23], s[20:21], s[22:23]
	s_nop 0
	v_cndmask_b32_e64 v4, v12, v4, s[22:23]
; __device__ __forceinline__ void p7_ffn_prep(const Ctx& C, bool dummy = false) {
;     ...
;             for (int k = 0; k < 4; ++k) { float best = -__builtin_inff(); int be = 0;
; #pragma unroll
;                 for (int e = 0; e < 32; ++e) { const bool taken = (k > 0 && e == e4[0]) || (k > 1 && e == e4[1]) || (k > 2 && e == e4[2]); if (!taken && v[e] > best) { best = v[e]; be = e; } }
;                 e4[k] = be; tv[k] = best; }
	v_cndmask_b32_e64 v6, 6, v6, s[22:23]
	v_cmp_eq_u32_e64 s[22:23], 7, v2
	v_cmp_ngt_f32_e64 s[24:25], v10, v4
	s_or_b64 s[24:25], s[22:23], s[24:25]
	s_nop 0
	v_cndmask_b32_e64 v4, v10, v4, s[24:25]
	v_cndmask_b32_e64 v6, 7, v6, s[24:25]
	v_cmp_eq_u32_e64 s[24:25], 8, v2
	v_cmp_ngt_f32_e64 s[26:27], v19, v4
	s_or_b64 s[26:27], s[24:25], s[26:27]
	s_nop 0
	v_cndmask_b32_e64 v4, v19, v4, s[26:27]
	v_cndmask_b32_e64 v6, 8, v6, s[26:27]
	v_cmp_eq_u32_e64 s[26:27], 9, v2
	v_cmp_ngt_f32_e64 s[28:29], v17, v4
	s_or_b64 s[28:29], s[26:27], s[28:29]
	s_nop 0
	v_cndmask_b32_e64 v4, v17, v4, s[28:29]
	v_cndmask_b32_e64 v6, 9, v6, s[28:29]
	v_cmp_eq_u32_e64 s[28:29], 10, v2
	v_cmp_ngt_f32_e64 s[30:31], v16, v4
	s_or_b64 s[30:31], s[28:29], s[30:31]
	s_nop 0
	v_cndmask_b32_e64 v4, v16, v4, s[30:31]
	v_cndmask_b32_e64 v6, 10, v6, s[30:31]
	v_cmp_eq_u32_e64 s[30:31], 11, v2
	v_cmp_ngt_f32_e64 s[34:35], v14, v4
	s_or_b64 s[34:35], s[30:31], s[34:35]
	s_nop 0
	v_cndmask_b32_e64 v4, v14, v4, s[34:35]
	v_cndmask_b32_e64 v6, 11, v6, s[34:35]
	v_cmp_eq_u32_e64 s[34:35], 12, v2
	v_cmp_ngt_f32_e64 s[36:37], v23, v4
	s_or_b64 s[36:37], s[34:35], s[36:37]
	s_nop 0
	v_cndmask_b32_e64 v4, v23, v4, s[36:37]
	v_cndmask_b32_e64 v6, 12, v6, s[36:37]
	v_cmp_eq_u32_e64 s[36:37], 13, v2
	v_cmp_ngt_f32_e64 s[38:39], v21, v4
	s_or_b64 s[38:39], s[36:37], s[38:39]
	s_nop 0
	v_cndmask_b32_e64 v4, v21, v4, s[38:39]
	v_cndmask_b32_e64 v6, 13, v6, s[38:39]
	v_cmp_eq_u32_e64 s[38:39], 14, v2
	v_cmp_ngt_f32_e64 s[40:41], v20, v4
	s_or_b64 s[40:41], s[38:39], s[40:41]
	s_nop 0
	v_cndmask_b32_e64 v4, v20, v4, s[40:41]
	v_cndmask_b32_e64 v6, 14, v6, s[40:41]
	v_cmp_eq_u32_e64 s[40:41], 15, v2
	v_cmp_ngt_f32_e64 s[42:43], v18, v4
	s_or_b64 s[42:43], s[40:41], s[42:43]
	s_nop 0
	v_cndmask_b32_e64 v4, v18, v4, s[42:43]
	v_cndmask_b32_e64 v6, 15, v6, s[42:43]
	v_cmp_eq_u32_e64 s[42:43], 16, v2
	v_cmp_ngt_f32_e64 s[44:45], v27, v4
	s_or_b64 s[44:45], s[42:43], s[44:45]
	s_nop 0
	v_cndmask_b32_e64 v4, v27, v4, s[44:45]
	v_cndmask_b32_e64 v6, 16, v6, s[44:45]
	v_cmp_eq_u32_e64 s[44:45], 17, v2
	v_cmp_ngt_f32_e64 s[46:47], v25, v4
	s_or_b64 s[46:47], s[44:45], s[46:47]
	s_nop 0
	v_cndmask_b32_e64 v4, v25, v4, s[46:47]
	v_cndmask_b32_e64 v6, 17, v6, s[46:47]
	v_cmp_eq_u32_e64 s[46:47], 18, v2
	v_cmp_ngt_f32_e64 s[48:49], v24, v4
	s_or_b64 s[48:49], s[46:47], s[48:49]
	s_nop 0
	v_cndmask_b32_e64 v4, v24, v4, s[48:49]
	v_cndmask_b32_e64 v6, 18, v6, s[48:49]
	v_cmp_eq_u32_e64 s[48:49], 19, v2
	v_cmp_ngt_f32_e64 s[50:51], v22, v4
	s_or_b64 s[50:51], s[48:49], s[50:51]
	s_nop 0
	v_cndmask_b32_e64 v4, v22, v4, s[50:51]
	v_cndmask_b32_e64 v6, 19, v6, s[50:51]
	v_cmp_eq_u32_e64 s[50:51], 20, v2
	v_cmp_ngt_f32_e64 s[52:53], v31, v4
	s_or_b64 s[52:53], s[50:51], s[52:53]
	s_nop 0
	v_cndmask_b32_e64 v4, v31, v4, s[52:53]
	v_cndmask_b32_e64 v6, 20, v6, s[52:53]
	v_cmp_eq_u32_e64 s[52:53], 21, v2
	v_cmp_ngt_f32_e64 s[54:55], v29, v4
	s_or_b64 s[54:55], s[52:53], s[54:55]
	s_nop 0
	v_cndmask_b32_e64 v4, v29, v4, s[54:55]
	v_cndmask_b32_e64 v6, 21, v6, s[54:55]
	v_cmp_eq_u32_e64 s[54:55], 22, v2
	v_cmp_ngt_f32_e64 s[56:57], v28, v4
	s_or_b64 s[56:57], s[54:55], s[56:57]
	s_nop 0
	v_cndmask_b32_e64 v4, v28, v4, s[56:57]
	v_cndmask_b32_e64 v6, 22, v6, s[56:57]
	v_cmp_eq_u32_e64 s[56:57], 23, v2
	v_cmp_ngt_f32_e64 s[58:59], v26, v4
	s_or_b64 s[58:59], s[56:57], s[58:59]
	s_nop 0
	v_cndmask_b32_e64 v4, v26, v4, s[58:59]
	v_cndmask_b32_e64 v6, 23, v6, s[58:59]
	v_cmp_eq_u32_e64 s[58:59], 24, v2
	v_cmp_ngt_f32_e64 s[60:61], v34, v4
	s_or_b64 s[60:61], s[58:59], s[60:61]
	s_nop 0
	v_cndmask_b32_e64 v4, v34, v4, s[60:61]
	v_cndmask_b32_e64 v6, 24, v6, s[60:61]
	v_cmp_eq_u32_e64 s[60:61], 25, v2
	v_cmp_ngt_f32_e64 s[62:63], v33, v4
	s_or_b64 s[62:63], s[60:61], s[62:63]
	s_nop 0
	v_cndmask_b32_e64 v4, v33, v4, s[62:63]
	v_cndmask_b32_e64 v6, 25, v6, s[62:63]
	v_cmp_eq_u32_e64 s[62:63], 26, v2
	v_cmp_ngt_f32_e64 s[64:65], v32, v4
	s_or_b64 s[64:65], s[62:63], s[64:65]
	s_nop 0
	v_cndmask_b32_e64 v4, v32, v4, s[64:65]
	v_cndmask_b32_e64 v6, 26, v6, s[64:65]
	v_cmp_eq_u32_e64 s[64:65], 27, v2
	v_cmp_ngt_f32_e64 s[66:67], v30, v4
	s_or_b64 s[66:67], s[64:65], s[66:67]
	s_nop 0
	v_cndmask_b32_e64 v4, v30, v4, s[66:67]
	v_cndmask_b32_e64 v6, 27, v6, s[66:67]
	v_cmp_eq_u32_e64 s[66:67], 28, v2
	v_cmp_ngt_f32_e64 s[68:69], v35, v4
	s_or_b64 s[68:69], s[66:67], s[68:69]
	s_nop 0
	v_cndmask_b32_e64 v4, v35, v4, s[68:69]
	v_cndmask_b32_e64 v6, 28, v6, s[68:69]
	v_cmp_ngt_f32_e64 s[68:69], v3, v4
	s_or_b64 s[68:69], s[72:73], s[68:69]
	s_nop 0
	v_cndmask_b32_e64 v4, v3, v4, s[68:69]
	v_cndmask_b32_e64 v6, 29, v6, s[68:69]
	v_cmp_ngt_f32_e64 s[68:69], v36, v4
	s_or_b64 s[68:69], s[70:71], s[68:69]
	s_nop 0
	v_cndmask_b32_e64 v4, v36, v4, s[68:69]
	v_cndmask_b32_e64 v6, 30, v6, s[68:69]
	v_cmp_eq_u32_e64 s[68:69], 31, v2
	v_cmp_ngt_f32_e64 s[74:75], v5, v4
	s_or_b64 s[74:75], s[68:69], s[74:75]
	s_nop 0
	v_cndmask_b32_e64 v38, v5, v4, s[74:75]
	v_cndmask_b32_e64 v4, 31, v6, s[74:75]
	v_cmp_eq_u32_e64 s[74:75], 0, v4
	s_or_b64 vcc, vcc, s[74:75]
	v_cndmask_b32_e32 v6, v11, v82, vcc
	v_cmp_eq_u32_e64 s[74:75], 1, v4
	s_or_b64 s[12:13], s[10:11], s[74:75]
	v_cmp_ngt_f32_e64 s[10:11], v9, v6
	s_or_b64 s[10:11], s[12:13], s[10:11]
	s_xor_b64 s[4:5], s[10:11], -1
	v_cndmask_b32_e64 v6, v9, v6, s[10:11]
	v_cmp_eq_u32_e64 s[10:11], 2, v4
	s_or_b64 s[14:15], s[0:1], s[10:11]
	v_cmp_ngt_f32_e64 s[10:11], v8, v6
	v_cndmask_b32_e64 v39, 0, 1, s[4:5]
	s_or_b64 s[10:11], s[14:15], s[10:11]
	v_cndmask_b32_e64 v6, v8, v6, s[10:11]
	v_cndmask_b32_e64 v39, 2, v39, s[10:11]
	v_cmp_eq_u32_e64 s[10:11], 3, v4
	s_or_b64 s[78:79], s[2:3], s[10:11]
; __device__ __forceinline__ void p7_ffn_prep(const Ctx& C, bool dummy = false) {
;     ...
;             for (int k = 0; k < 4; ++k) { float best = -__builtin_inff(); int be = 0;
; #pragma unroll
;                 for (int e = 0; e < 32; ++e) { const bool taken = (k > 0 && e == e4[0]) || (k > 1 && e == e4[1]) || (k > 2 && e == e4[2]); if (!taken && v[e] > best) { best = v[e]; be = e; } }
;                 e4[k] = be; tv[k] = best; }
	v_cmp_ngt_f32_e64 s[10:11], v7, v6
	s_or_b64 s[10:11], s[78:79], s[10:11]
	s_nop 0
	v_cndmask_b32_e64 v6, v7, v6, s[10:11]
	v_cndmask_b32_e64 v39, 3, v39, s[10:11]
	v_cmp_eq_u32_e64 s[10:11], 4, v4
	s_or_b64 s[76:77], s[16:17], s[10:11]
	v_cmp_ngt_f32_e64 s[10:11], v15, v6
	s_or_b64 s[10:11], s[76:77], s[10:11]
	s_nop 0
	v_cndmask_b32_e64 v6, v15, v6, s[10:11]
	v_cndmask_b32_e64 v39, 4, v39, s[10:11]
	v_cmp_eq_u32_e64 s[10:11], 5, v4
	s_or_b64 s[0:1], s[18:19], s[10:11]
	v_cmp_ngt_f32_e64 s[10:11], v13, v6
	s_or_b64 s[10:11], s[0:1], s[10:11]
	s_xor_b64 s[0:1], s[0:1], -1
	v_cndmask_b32_e64 v6, v13, v6, s[10:11]
	v_cndmask_b32_e64 v39, 5, v39, s[10:11]
	v_cmp_eq_u32_e64 s[10:11], 6, v4
	s_or_b64 s[2:3], s[20:21], s[10:11]
	v_cmp_ngt_f32_e64 s[10:11], v12, v6
	s_or_b64 s[10:11], s[2:3], s[10:11]
	s_nop 0
	v_cndmask_b32_e64 v6, v12, v6, s[10:11]
	v_cndmask_b32_e64 v39, 6, v39, s[10:11]
	v_cmp_eq_u32_e64 s[10:11], 7, v4
	s_or_b64 s[96:97], s[22:23], s[10:11]
	v_cmp_ngt_f32_e64 s[10:11], v10, v6
	s_or_b64 s[10:11], s[96:97], s[10:11]
	s_nop 0
	v_cndmask_b32_e64 v6, v10, v6, s[10:11]
	v_cndmask_b32_e64 v39, 7, v39, s[10:11]
	v_cmp_eq_u32_e64 s[10:11], 8, v4
	s_or_b64 s[94:95], s[24:25], s[10:11]
	v_cmp_ngt_f32_e64 s[10:11], v19, v6
	s_or_b64 s[10:11], s[94:95], s[10:11]
	s_nop 0
	v_cndmask_b32_e64 v6, v19, v6, s[10:11]
	v_cndmask_b32_e64 v39, 8, v39, s[10:11]
	v_cmp_eq_u32_e64 s[10:11], 9, v4
	s_or_b64 s[8:9], s[26:27], s[10:11]
	v_cmp_ngt_f32_e64 s[10:11], v17, v6
	s_or_b64 s[10:11], s[8:9], s[10:11]
	s_nop 0
	v_cndmask_b32_e64 v6, v17, v6, s[10:11]
	v_cndmask_b32_e64 v39, 9, v39, s[10:11]
	v_cmp_eq_u32_e64 s[10:11], 10, v4
	s_or_b64 s[6:7], s[28:29], s[10:11]
	v_cmp_ngt_f32_e64 s[10:11], v16, v6
	s_or_b64 s[10:11], s[6:7], s[10:11]
	s_nop 0
	v_cndmask_b32_e64 v6, v16, v6, s[10:11]
	v_cndmask_b32_e64 v39, 10, v39, s[10:11]
	v_cmp_eq_u32_e64 s[10:11], 11, v4
	s_or_b64 s[80:81], s[30:31], s[10:11]
	v_cmp_ngt_f32_e64 s[10:11], v14, v6
	s_or_b64 s[10:11], s[80:81], s[10:11]
	s_nop 0
	v_cndmask_b32_e64 v6, v14, v6, s[10:11]
	v_cndmask_b32_e64 v39, 11, v39, s[10:11]
	v_cmp_eq_u32_e64 s[10:11], 12, v4
	s_or_b64 s[92:93], s[34:35], s[10:11]
	v_cmp_ngt_f32_e64 s[10:11], v23, v6
	s_or_b64 s[10:11], s[92:93], s[10:11]
	s_nop 0
	v_cndmask_b32_e64 v6, v23, v6, s[10:11]
	v_cndmask_b32_e64 v39, 12, v39, s[10:11]
	v_cmp_eq_u32_e64 s[10:11], 13, v4
	s_or_b64 s[18:19], s[36:37], s[10:11]
	v_cmp_ngt_f32_e64 s[10:11], v21, v6
	s_or_b64 s[10:11], s[18:19], s[10:11]
	s_nop 0
	v_cndmask_b32_e64 v6, v21, v6, s[10:11]
	v_cndmask_b32_e64 v39, 13, v39, s[10:11]
	v_cmp_eq_u32_e64 s[10:11], 14, v4
	s_or_b64 s[4:5], s[38:39], s[10:11]
	v_cmp_ngt_f32_e64 s[10:11], v20, v6
	s_or_b64 s[10:11], s[4:5], s[10:11]
	s_nop 0
	v_cndmask_b32_e64 v6, v20, v6, s[10:11]
	v_cndmask_b32_e64 v39, 14, v39, s[10:11]
	v_cmp_eq_u32_e64 s[10:11], 15, v4
	s_or_b64 s[16:17], s[40:41], s[10:11]
	v_cmp_ngt_f32_e64 s[10:11], v18, v6
	s_or_b64 s[10:11], s[16:17], s[10:11]
	s_nop 0
	v_cndmask_b32_e64 v6, v18, v6, s[10:11]
	v_cndmask_b32_e64 v39, 15, v39, s[10:11]
	v_cmp_eq_u32_e64 s[10:11], 16, v4
	s_or_b64 s[74:75], s[42:43], s[10:11]
	v_cmp_ngt_f32_e64 s[10:11], v27, v6
	s_or_b64 s[10:11], s[74:75], s[10:11]
	s_nop 0
	v_cndmask_b32_e64 v6, v27, v6, s[10:11]
	v_cndmask_b32_e64 v39, 16, v39, s[10:11]
	v_cmp_eq_u32_e64 s[10:11], 17, v4
	s_or_b64 s[42:43], s[44:45], s[10:11]
	v_cmp_ngt_f32_e64 s[10:11], v25, v6
	s_or_b64 s[10:11], s[42:43], s[10:11]
	s_nop 0
	v_cndmask_b32_e64 v6, v25, v6, s[10:11]
	v_cndmask_b32_e64 v39, 17, v39, s[10:11]
	v_cmp_eq_u32_e64 s[10:11], 18, v4
	s_or_b64 s[40:41], s[46:47], s[10:11]
	v_cmp_ngt_f32_e64 s[10:11], v24, v6
	s_or_b64 s[10:11], s[40:41], s[10:11]
	s_nop 0
	v_cndmask_b32_e64 v6, v24, v6, s[10:11]
	v_cndmask_b32_e64 v39, 18, v39, s[10:11]
	v_cmp_eq_u32_e64 s[10:11], 19, v4
	s_or_b64 s[38:39], s[48:49], s[10:11]
	v_cmp_ngt_f32_e64 s[10:11], v22, v6
	s_or_b64 s[10:11], s[38:39], s[10:11]
	s_nop 0
	v_cndmask_b32_e64 v6, v22, v6, s[10:11]
	v_cndmask_b32_e64 v39, 19, v39, s[10:11]
	v_cmp_eq_u32_e64 s[10:11], 20, v4
	s_or_b64 s[36:37], s[50:51], s[10:11]
	v_cmp_ngt_f32_e64 s[10:11], v31, v6
	s_or_b64 s[10:11], s[36:37], s[10:11]
	s_nop 0
	v_cndmask_b32_e64 v6, v31, v6, s[10:11]
	v_cndmask_b32_e64 v39, 20, v39, s[10:11]
	v_cmp_eq_u32_e64 s[10:11], 21, v4
	s_or_b64 s[34:35], s[52:53], s[10:11]
	v_cmp_ngt_f32_e64 s[10:11], v29, v6
	s_or_b64 s[10:11], s[34:35], s[10:11]
	s_nop 0
	v_cndmask_b32_e64 v6, v29, v6, s[10:11]
	v_cndmask_b32_e64 v39, 21, v39, s[10:11]
	v_cmp_eq_u32_e64 s[10:11], 22, v4
	s_or_b64 s[30:31], s[54:55], s[10:11]
	v_cmp_ngt_f32_e64 s[10:11], v28, v6
	s_or_b64 s[10:11], s[30:31], s[10:11]
	s_nop 0
	v_cndmask_b32_e64 v6, v28, v6, s[10:11]
	v_cndmask_b32_e64 v39, 22, v39, s[10:11]
	v_cmp_eq_u32_e64 s[10:11], 23, v4
	s_or_b64 s[28:29], s[56:57], s[10:11]
	v_cmp_ngt_f32_e64 s[10:11], v26, v6
	s_or_b64 s[10:11], s[28:29], s[10:11]
	s_nop 0
	v_cndmask_b32_e64 v6, v26, v6, s[10:11]
	v_cndmask_b32_e64 v39, 23, v39, s[10:11]
	v_cmp_eq_u32_e64 s[10:11], 24, v4
	s_or_b64 s[26:27], s[58:59], s[10:11]
	v_cmp_ngt_f32_e64 s[10:11], v34, v6
	s_or_b64 s[10:11], s[26:27], s[10:11]
	s_nop 0
	v_cndmask_b32_e64 v6, v34, v6, s[10:11]
	v_cndmask_b32_e64 v39, 24, v39, s[10:11]
	v_cmp_eq_u32_e64 s[10:11], 25, v4
	s_or_b64 s[24:25], s[60:61], s[10:11]
	v_cmp_ngt_f32_e64 s[10:11], v33, v6
	s_or_b64 s[10:11], s[24:25], s[10:11]
	s_nop 0
	v_cndmask_b32_e64 v6, v33, v6, s[10:11]
	v_cndmask_b32_e64 v39, 25, v39, s[10:11]
	v_cmp_eq_u32_e64 s[10:11], 26, v4
	s_or_b64 s[22:23], s[62:63], s[10:11]
	v_cmp_ngt_f32_e64 s[10:11], v32, v6
	s_or_b64 s[10:11], s[22:23], s[10:11]
; __device__ __forceinline__ void p7_ffn_prep(const Ctx& C, bool dummy = false) {
;     ...
;             for (int k = 0; k < 4; ++k) { float best = -__builtin_inff(); int be = 0;
; #pragma unroll
;                 for (int e = 0; e < 32; ++e) { const bool taken = (k > 0 && e == e4[0]) || (k > 1 && e == e4[1]) || (k > 2 && e == e4[2]); if (!taken && v[e] > best) { best = v[e]; be = e; } }
;                 e4[k] = be; tv[k] = best; }
	v_readlane_b32 s60, v254, 8
	v_cndmask_b32_e64 v6, v32, v6, s[10:11]
	v_cndmask_b32_e64 v39, 26, v39, s[10:11]
	v_cmp_eq_u32_e64 s[10:11], 27, v4
	s_or_b64 s[20:21], s[64:65], s[10:11]
	v_cmp_ngt_f32_e64 s[10:11], v30, v6
	s_or_b64 s[10:11], s[20:21], s[10:11]
	v_readlane_b32 s61, v254, 9
	v_cndmask_b32_e64 v6, v30, v6, s[10:11]
	v_cndmask_b32_e64 v39, 27, v39, s[10:11]
	v_cmp_eq_u32_e64 s[10:11], 28, v4
	s_or_b64 s[50:51], s[66:67], s[10:11]
	v_cmp_ngt_f32_e64 s[10:11], v35, v6
	s_or_b64 s[10:11], s[50:51], s[10:11]
	v_readlane_b32 s62, v254, 10
	v_cndmask_b32_e64 v6, v35, v6, s[10:11]
	v_cndmask_b32_e64 v39, 28, v39, s[10:11]
	v_cmp_eq_u32_e64 s[10:11], 29, v4
	s_or_b64 s[48:49], s[72:73], s[10:11]
	v_cmp_ngt_f32_e64 s[10:11], v3, v6
	s_or_b64 s[10:11], s[48:49], s[10:11]
	v_readlane_b32 s63, v254, 11
	v_cndmask_b32_e64 v6, v3, v6, s[10:11]
	v_cndmask_b32_e64 v39, 29, v39, s[10:11]
	v_cmp_eq_u32_e64 s[10:11], 30, v4
	s_or_b64 s[46:47], s[70:71], s[10:11]
	v_cmp_ngt_f32_e64 s[10:11], v36, v6
	s_or_b64 s[10:11], s[46:47], s[10:11]
	s_nop 0
	v_cndmask_b32_e64 v6, v36, v6, s[10:11]
	v_cndmask_b32_e64 v39, 30, v39, s[10:11]
	v_cmp_eq_u32_e64 s[10:11], 31, v4
	s_or_b64 s[44:45], s[68:69], s[10:11]
	v_cmp_ngt_f32_e64 s[10:11], v5, v6
	s_or_b64 s[10:11], s[44:45], s[10:11]
	s_nop 0
	v_cndmask_b32_e64 v40, v5, v6, s[10:11]
	v_cndmask_b32_e64 v6, 31, v39, s[10:11]
	v_cmp_eq_u32_e64 s[10:11], 0, v6
	s_or_b64 vcc, vcc, s[10:11]
	v_cndmask_b32_e32 v11, v11, v82, vcc
	v_cmp_ne_u32_e32 vcc, 1, v6
	s_xor_b64 s[10:11], s[12:13], -1
	s_and_b64 s[10:11], s[10:11], vcc
	v_cmp_gt_f32_e32 vcc, v9, v11
	s_and_b64 vcc, s[10:11], vcc
	s_xor_b64 s[10:11], s[14:15], -1
	v_cndmask_b32_e32 v9, v11, v9, vcc
	v_cndmask_b32_e64 v11, 0, 1, vcc
	v_cmp_ne_u32_e32 vcc, 2, v6
	s_and_b64 s[10:11], s[10:11], vcc
	v_cmp_gt_f32_e32 vcc, v8, v9
	s_and_b64 vcc, s[10:11], vcc
	s_xor_b64 s[10:11], s[78:79], -1
	v_cndmask_b32_e32 v8, v9, v8, vcc
	v_cndmask_b32_e64 v9, v11, 2, vcc
	v_cmp_ne_u32_e32 vcc, 3, v6
	s_and_b64 s[10:11], s[10:11], vcc
	v_cmp_gt_f32_e32 vcc, v7, v8
	s_and_b64 vcc, s[10:11], vcc
	s_xor_b64 s[10:11], s[76:77], -1
	v_cndmask_b32_e32 v7, v8, v7, vcc
	v_cndmask_b32_e64 v8, v9, 3, vcc
	v_cmp_ne_u32_e32 vcc, 4, v6
	s_and_b64 s[10:11], s[10:11], vcc
	v_cmp_gt_f32_e32 vcc, v15, v7
	s_and_b64 vcc, s[10:11], vcc
	s_nop 0
	v_cndmask_b32_e32 v7, v7, v15, vcc
	v_cndmask_b32_e64 v8, v8, 4, vcc
	v_cmp_ne_u32_e32 vcc, 5, v6
	s_and_b64 s[0:1], s[0:1], vcc
	v_cmp_gt_f32_e32 vcc, v13, v7
	s_and_b64 vcc, s[0:1], vcc
	s_xor_b64 s[0:1], s[2:3], -1
	v_cndmask_b32_e32 v7, v7, v13, vcc
	v_cndmask_b32_e64 v8, v8, 5, vcc
	v_cmp_ne_u32_e32 vcc, 6, v6
	s_and_b64 s[0:1], s[0:1], vcc
	v_cmp_gt_f32_e32 vcc, v12, v7
	s_and_b64 vcc, s[0:1], vcc
	s_xor_b64 s[0:1], s[96:97], -1
	v_cndmask_b32_e32 v7, v7, v12, vcc
	v_cndmask_b32_e64 v8, v8, 6, vcc
	v_cmp_ne_u32_e32 vcc, 7, v6
	s_and_b64 s[0:1], s[0:1], vcc
	v_cmp_gt_f32_e32 vcc, v10, v7
	s_and_b64 vcc, s[0:1], vcc
	s_xor_b64 s[0:1], s[94:95], -1
	v_cndmask_b32_e32 v7, v7, v10, vcc
	v_cndmask_b32_e64 v8, v8, 7, vcc
	v_cmp_ne_u32_e32 vcc, 8, v6
	s_and_b64 s[0:1], s[0:1], vcc
	v_cmp_gt_f32_e32 vcc, v19, v7
	s_and_b64 vcc, s[0:1], vcc
	s_xor_b64 s[0:1], s[8:9], -1
	v_cndmask_b32_e32 v7, v7, v19, vcc
	v_cndmask_b32_e64 v8, v8, 8, vcc
	v_cmp_ne_u32_e32 vcc, 9, v6
	s_and_b64 s[0:1], s[0:1], vcc
	v_cmp_gt_f32_e32 vcc, v17, v7
	s_and_b64 vcc, s[0:1], vcc
	s_xor_b64 s[0:1], s[6:7], -1
	v_cndmask_b32_e32 v7, v7, v17, vcc
	v_cndmask_b32_e64 v8, v8, 9, vcc
	v_cmp_ne_u32_e32 vcc, 10, v6
	s_and_b64 s[0:1], s[0:1], vcc
	v_cmp_gt_f32_e32 vcc, v16, v7
	s_and_b64 vcc, s[0:1], vcc
	s_xor_b64 s[0:1], s[80:81], -1
	v_cndmask_b32_e32 v7, v7, v16, vcc
	v_cndmask_b32_e64 v8, v8, 10, vcc
	v_cmp_ne_u32_e32 vcc, 11, v6
	s_and_b64 s[0:1], s[0:1], vcc
	v_cmp_gt_f32_e32 vcc, v14, v7
	s_and_b64 vcc, s[0:1], vcc
	s_xor_b64 s[0:1], s[92:93], -1
	v_cndmask_b32_e32 v7, v7, v14, vcc
	v_cndmask_b32_e64 v8, v8, 11, vcc
	v_cmp_ne_u32_e32 vcc, 12, v6
	s_and_b64 s[0:1], s[0:1], vcc
	v_cmp_gt_f32_e32 vcc, v23, v7
	s_and_b64 vcc, s[0:1], vcc
	s_xor_b64 s[0:1], s[18:19], -1
	v_cndmask_b32_e32 v7, v7, v23, vcc
	v_cndmask_b32_e64 v8, v8, 12, vcc
	v_cmp_ne_u32_e32 vcc, 13, v6
	s_and_b64 s[0:1], s[0:1], vcc
	v_cmp_gt_f32_e32 vcc, v21, v7
	s_and_b64 vcc, s[0:1], vcc
	s_xor_b64 s[0:1], s[4:5], -1
	v_cndmask_b32_e32 v7, v7, v21, vcc
	v_cndmask_b32_e64 v8, v8, 13, vcc
	v_cmp_ne_u32_e32 vcc, 14, v6
	s_and_b64 s[0:1], s[0:1], vcc
	v_cmp_gt_f32_e32 vcc, v20, v7
	s_and_b64 vcc, s[0:1], vcc
	s_xor_b64 s[0:1], s[16:17], -1
	v_cndmask_b32_e32 v7, v7, v20, vcc
	v_cndmask_b32_e64 v8, v8, 14, vcc
	v_cmp_ne_u32_e32 vcc, 15, v6
	s_and_b64 s[0:1], s[0:1], vcc
; __device__ __forceinline__ void p7_ffn_prep(const Ctx& C, bool dummy = false) {
;     ...
;             for (int k = 0; k < 4; ++k) { float best = -__builtin_inff(); int be = 0;
; #pragma unroll
;                 for (int e = 0; e < 32; ++e) { const bool taken = (k > 0 && e == e4[0]) || (k > 1 && e == e4[1]) || (k > 2 && e == e4[2]); if (!taken && v[e] > best) { best = v[e]; be = e; } }
;                 e4[k] = be; tv[k] = best; }
;             const float p1 = __expf(tv[1] - tv[0]), p2 = __expf(tv[2] - tv[0]), p3 = __expf(tv[3] - tv[0]); const float inv = 1.0f / (1.0f + p1 + p2 + p3);
;             gk[0] = inv; gk[1] = p1 * inv; gk[2] = p2 * inv; gk[3] = p3 * inv;
; #pragma unroll
;             for (int k = 0; k < 4; ++k) rk[k] = __hip_atomic_fetch_add(cnt + e4[k], 1, __ATOMIC_RELAXED, __HIP_MEMORY_SCOPE_WORKGROUP);
	v_cmp_gt_f32_e32 vcc, v18, v7
	s_and_b64 vcc, s[0:1], vcc
	s_xor_b64 s[0:1], s[74:75], -1
	v_cndmask_b32_e32 v7, v7, v18, vcc
	v_cndmask_b32_e64 v8, v8, 15, vcc
	v_cmp_ne_u32_e32 vcc, 16, v6
	s_and_b64 s[0:1], s[0:1], vcc
	v_cmp_gt_f32_e32 vcc, v27, v7
	s_and_b64 vcc, s[0:1], vcc
	s_xor_b64 s[0:1], s[42:43], -1
	v_cndmask_b32_e32 v7, v7, v27, vcc
	v_cndmask_b32_e64 v8, v8, 16, vcc
	v_cmp_ne_u32_e32 vcc, 17, v6
	s_and_b64 s[0:1], s[0:1], vcc
	v_cmp_gt_f32_e32 vcc, v25, v7
	s_and_b64 vcc, s[0:1], vcc
	s_xor_b64 s[0:1], s[40:41], -1
	v_cndmask_b32_e32 v7, v7, v25, vcc
	v_cndmask_b32_e64 v8, v8, 17, vcc
	v_cmp_ne_u32_e32 vcc, 18, v6
	s_and_b64 s[0:1], s[0:1], vcc
	v_cmp_gt_f32_e32 vcc, v24, v7
	s_and_b64 vcc, s[0:1], vcc
	s_xor_b64 s[0:1], s[38:39], -1
	v_cndmask_b32_e32 v7, v7, v24, vcc
	v_cndmask_b32_e64 v8, v8, 18, vcc
	v_cmp_ne_u32_e32 vcc, 19, v6
	s_and_b64 s[0:1], s[0:1], vcc
	v_cmp_gt_f32_e32 vcc, v22, v7
	s_and_b64 vcc, s[0:1], vcc
	s_xor_b64 s[0:1], s[36:37], -1
	v_cndmask_b32_e32 v7, v7, v22, vcc
	v_cndmask_b32_e64 v8, v8, 19, vcc
	v_cmp_ne_u32_e32 vcc, 20, v6
	s_and_b64 s[0:1], s[0:1], vcc
	v_cmp_gt_f32_e32 vcc, v31, v7
	s_and_b64 vcc, s[0:1], vcc
	s_xor_b64 s[0:1], s[34:35], -1
	v_cndmask_b32_e32 v7, v7, v31, vcc
	v_cndmask_b32_e64 v8, v8, 20, vcc
	v_cmp_ne_u32_e32 vcc, 21, v6
	s_and_b64 s[0:1], s[0:1], vcc
	v_cmp_gt_f32_e32 vcc, v29, v7
	s_and_b64 vcc, s[0:1], vcc
	s_xor_b64 s[0:1], s[30:31], -1
	v_cndmask_b32_e32 v7, v7, v29, vcc
	v_cndmask_b32_e64 v8, v8, 21, vcc
	v_cmp_ne_u32_e32 vcc, 22, v6
	s_and_b64 s[0:1], s[0:1], vcc
	v_cmp_gt_f32_e32 vcc, v28, v7
	s_and_b64 vcc, s[0:1], vcc
	s_xor_b64 s[0:1], s[28:29], -1
	v_cndmask_b32_e32 v7, v7, v28, vcc
	v_cndmask_b32_e64 v8, v8, 22, vcc
	v_cmp_ne_u32_e32 vcc, 23, v6
	s_and_b64 s[0:1], s[0:1], vcc
	v_cmp_gt_f32_e32 vcc, v26, v7
	s_and_b64 vcc, s[0:1], vcc
	s_xor_b64 s[0:1], s[26:27], -1
	v_cndmask_b32_e32 v7, v7, v26, vcc
	v_cndmask_b32_e64 v8, v8, 23, vcc
	v_cmp_ne_u32_e32 vcc, 24, v6
	s_and_b64 s[0:1], s[0:1], vcc
	v_cmp_gt_f32_e32 vcc, v34, v7
	s_and_b64 vcc, s[0:1], vcc
	s_xor_b64 s[0:1], s[24:25], -1
	v_cndmask_b32_e32 v7, v7, v34, vcc
	v_cndmask_b32_e64 v8, v8, 24, vcc
	v_cmp_ne_u32_e32 vcc, 25, v6
	s_and_b64 s[0:1], s[0:1], vcc
	v_cmp_gt_f32_e32 vcc, v33, v7
	s_and_b64 vcc, s[0:1], vcc
	s_xor_b64 s[0:1], s[22:23], -1
	v_cndmask_b32_e32 v7, v7, v33, vcc
	v_cndmask_b32_e64 v8, v8, 25, vcc
	v_cmp_ne_u32_e32 vcc, 26, v6
	s_and_b64 s[0:1], s[0:1], vcc
	v_cmp_gt_f32_e32 vcc, v32, v7
	s_and_b64 vcc, s[0:1], vcc
	s_xor_b64 s[0:1], s[20:21], -1
	v_cndmask_b32_e32 v7, v7, v32, vcc
	v_cndmask_b32_e64 v8, v8, 26, vcc
	v_cmp_ne_u32_e32 vcc, 27, v6
	s_and_b64 s[0:1], s[0:1], vcc
	v_cmp_gt_f32_e32 vcc, v30, v7
	s_and_b64 vcc, s[0:1], vcc
	s_xor_b64 s[0:1], s[50:51], -1
	v_cndmask_b32_e32 v7, v7, v30, vcc
	v_cndmask_b32_e64 v8, v8, 27, vcc
	v_cmp_ne_u32_e32 vcc, 28, v6
	s_and_b64 s[0:1], s[0:1], vcc
	v_cmp_gt_f32_e32 vcc, v35, v7
	s_and_b64 vcc, s[0:1], vcc
	s_xor_b64 s[0:1], s[48:49], -1
	v_cndmask_b32_e32 v7, v7, v35, vcc
	v_cndmask_b32_e64 v8, v8, 28, vcc
	v_cmp_ne_u32_e32 vcc, 29, v6
	s_and_b64 s[0:1], s[0:1], vcc
	v_cmp_gt_f32_e32 vcc, v3, v7
	s_and_b64 vcc, s[0:1], vcc
	s_xor_b64 s[0:1], s[46:47], -1
	v_cndmask_b32_e32 v3, v7, v3, vcc
	v_cndmask_b32_e64 v7, v8, 29, vcc
	v_cmp_ne_u32_e32 vcc, 30, v6
	s_and_b64 s[0:1], s[0:1], vcc
	v_cmp_gt_f32_e32 vcc, v36, v3
	s_and_b64 vcc, s[0:1], vcc
	s_xor_b64 s[0:1], s[44:45], -1
	v_cndmask_b32_e32 v3, v3, v36, vcc
	v_cndmask_b32_e64 v7, v7, 30, vcc
	v_cmp_ne_u32_e32 vcc, 31, v6
	s_and_b64 s[0:1], s[0:1], vcc
	v_cmp_gt_f32_e32 vcc, v5, v3
	s_and_b64 vcc, s[0:1], vcc
	s_nop 0
	v_cndmask_b32_e32 v3, v3, v5, vcc
	v_sub_f32_e32 v5, v38, v37
	v_mul_f32_e32 v5, 0x3fb8aa3b, v5
	v_exp_f32_e32 v10, v5
	v_sub_f32_e32 v5, v40, v37
	v_mul_f32_e32 v5, 0x3fb8aa3b, v5
	v_sub_f32_e32 v3, v3, v37
	v_exp_f32_e32 v11, v5
	v_mul_f32_e32 v3, 0x3fb8aa3b, v3
	v_exp_f32_e32 v3, v3
	v_add_f32_e32 v5, 1.0, v10
	v_add_f32_e32 v5, v5, v11
	v_cndmask_b32_e64 v8, v7, 31, vcc
	v_add_f32_e32 v5, v5, v3
	v_div_scale_f32 v7, s[0:1], v5, v5, 1.0
	v_rcp_f32_e32 v9, v7
	s_nop 0
	v_fma_f32 v12, -v7, v9, 1.0
	v_fmac_f32_e32 v9, v12, v9
	v_div_scale_f32 v12, vcc, 1.0, v5, 1.0
	v_mul_f32_e32 v13, v12, v9
	v_fma_f32 v14, -v7, v13, v12
	v_fmac_f32_e32 v13, v14, v9
	v_fma_f32 v7, -v7, v13, v12
	v_div_fmas_f32 v7, v7, v9, v13
	v_div_fixup_f32 v12, v7, v5, 1.0
	v_pk_mul_f32 v[10:11], v[10:11], v[12:13] op_sel_hi:[1,0]
	v_mul_f32_e32 v13, v3, v12
	v_lshl_add_u32 v3, v2, 2, 0
	ds_add_rtn_u32 v20, v3, v80
	v_lshl_add_u32 v3, v4, 2, 0
	ds_add_rtn_u32 v18, v3, v80
	v_lshl_add_u32 v3, v6, 2, 0
	ds_add_rtn_u32 v16, v3, v80
	v_lshl_add_u32 v3, v8, 2, 0
	ds_add_rtn_u32 v14, v3, v80
